# norm2 router GEMV: LDS weight reads of the first four column groups rotate through three dead buffers, two reads ahead, counted lgkmcnt (were lgkmcnt(0) / one ahead)
# baseline (speedup 1.0000x reference)
.LBB0_1300:
	v_lshl_add_u64 v[2:3], s[58:59], 0, v[60:61]
	v_add_co_u32_e32 v4, vcc, 0x11100000, v2
	v_lshl_add_u64 v[158:159], s[58:59], 0, v[58:59]
	s_nop 0
	v_addc_co_u32_e32 v5, vcc, 0, v3, vcc
	global_load_dwordx2 v[94:95], v[4:5], off nt
	v_add_co_u32_e32 v96, vcc, 0x11101000, v2
	s_nop 1
	v_addc_co_u32_e32 v97, vcc, 0, v3, vcc
	global_load_dwordx2 v[98:99], v[96:97], off nt
	global_load_dwordx2 v[100:101], v[4:5], off offset:512 nt
	global_load_dwordx2 v[106:107], v[96:97], off offset:512 nt
	global_load_dwordx2 v[108:109], v[4:5], off offset:1024 nt
	global_load_dwordx2 v[110:111], v[96:97], off offset:1024 nt
	global_load_dwordx2 v[20:21], v[4:5], off offset:1536 nt
	global_load_dwordx2 v[18:19], v[96:97], off offset:1536 nt
	global_load_dwordx2 v[16:17], v[4:5], off offset:2048 nt
	global_load_dwordx2 v[14:15], v[96:97], off offset:2048 nt
	global_load_dwordx2 v[12:13], v[4:5], off offset:2560 nt
	global_load_dwordx2 v[10:11], v[96:97], off offset:2560 nt
	global_load_dwordx2 v[8:9], v[4:5], off offset:3072 nt
	global_load_dwordx2 v[6:7], v[96:97], off offset:3072 nt
	global_load_dwordx2 v[2:3], v[4:5], off offset:3584 nt
	s_nop 0
	global_load_dwordx2 v[4:5], v[96:97], off offset:3584 nt
	s_waitcnt vmcnt(15)
	v_and_b32_e32 v157, 0xffff0000, v94
	v_and_b32_e32 v155, 0xffff0000, v95
	v_lshlrev_b32_e32 v156, 16, v94
	v_lshlrev_b32_e32 v154, 16, v95
	v_mul_f32_e32 v47, v157, v157
	v_mul_f32_e32 v49, v155, v155
	v_fmac_f32_e32 v47, v156, v156
	v_fmac_f32_e32 v49, v154, v154
	v_add_f32_e32 v47, v47, v49
	s_waitcnt vmcnt(14)
	v_and_b32_e32 v153, 0xffff0000, v98
	v_and_b32_e32 v119, 0xffff0000, v99
	v_lshlrev_b32_e32 v152, 16, v98
	v_lshlrev_b32_e32 v118, 16, v99
	v_mul_f32_e32 v49, v153, v153
	v_mul_f32_e32 v51, v119, v119
	v_fmac_f32_e32 v49, v152, v152
	v_fmac_f32_e32 v51, v118, v118
	s_waitcnt vmcnt(13)
	v_and_b32_e32 v151, 0xffff0000, v100
	v_and_b32_e32 v149, 0xffff0000, v101
	v_add_f32_e32 v49, v49, v51
	v_lshlrev_b32_e32 v150, 16, v100
	v_lshlrev_b32_e32 v148, 16, v101
	v_mul_f32_e32 v51, v151, v151
	v_mul_f32_e32 v53, v149, v149
	v_fmac_f32_e32 v51, v150, v150
	v_fmac_f32_e32 v53, v148, v148
	s_waitcnt vmcnt(12)
	v_and_b32_e32 v147, 0xffff0000, v106
	v_and_b32_e32 v145, 0xffff0000, v107
	v_add_f32_e32 v51, v51, v53
	v_lshlrev_b32_e32 v146, 16, v106
	v_lshlrev_b32_e32 v144, 16, v107
	v_add_f32_e32 v47, v47, v51
	v_mul_f32_e32 v51, v147, v147
	v_mul_f32_e32 v53, v145, v145
	v_fmac_f32_e32 v51, v146, v146
	v_fmac_f32_e32 v53, v144, v144
	v_add_f32_e32 v51, v51, v53
	s_waitcnt vmcnt(11)
	v_and_b32_e32 v143, 0xffff0000, v108
	v_and_b32_e32 v141, 0xffff0000, v109
	v_add_f32_e32 v49, v49, v51
	v_lshlrev_b32_e32 v142, 16, v108
	v_lshlrev_b32_e32 v140, 16, v109
	v_mul_f32_e32 v51, v143, v143
	v_mul_f32_e32 v53, v141, v141
	v_fmac_f32_e32 v51, v142, v142
	v_fmac_f32_e32 v53, v140, v140
	s_waitcnt vmcnt(9)
	v_and_b32_e32 v131, 0xffff0000, v20
	v_and_b32_e32 v129, 0xffff0000, v21
	v_and_b32_e32 v139, 0xffff0000, v110
	v_and_b32_e32 v137, 0xffff0000, v111
	v_add_f32_e32 v51, v51, v53
	v_lshlrev_b32_e32 v130, 16, v20
	v_lshlrev_b32_e32 v128, 16, v21
	s_waitcnt vmcnt(8)
	v_lshlrev_b32_e32 v132, 16, v18
	v_and_b32_e32 v133, 0xffff0000, v18
	v_lshlrev_b32_e32 v134, 16, v19
	v_and_b32_e32 v135, 0xffff0000, v19
	v_mul_f32_e32 v18, v131, v131
	v_mul_f32_e32 v19, v129, v129
	s_waitcnt vmcnt(7)
	v_and_b32_e32 v127, 0xffff0000, v16
	v_and_b32_e32 v125, 0xffff0000, v17
	v_lshlrev_b32_e32 v138, 16, v110
	v_lshlrev_b32_e32 v136, 16, v111
	v_add_f32_e32 v47, v47, v51
	v_mul_f32_e32 v51, v139, v139
	v_mul_f32_e32 v53, v137, v137
	v_fmac_f32_e32 v18, v130, v130
	v_fmac_f32_e32 v19, v128, v128
	v_lshlrev_b32_e32 v126, 16, v16
	v_lshlrev_b32_e32 v124, 16, v17
	s_waitcnt vmcnt(6)
	v_lshlrev_b32_e32 v122, 16, v14
	v_and_b32_e32 v123, 0xffff0000, v14
	v_lshlrev_b32_e32 v120, 16, v15
	v_and_b32_e32 v121, 0xffff0000, v15
	v_mul_f32_e32 v14, v127, v127
	v_mul_f32_e32 v15, v125, v125
	v_fmac_f32_e32 v51, v138, v138
	v_fmac_f32_e32 v53, v136, v136
	v_add_f32_e32 v18, v18, v19
	v_mul_f32_e32 v19, v133, v133
	v_mul_f32_e32 v20, v135, v135
	v_fmac_f32_e32 v14, v126, v126
	v_fmac_f32_e32 v15, v124, v124
	v_add_f32_e32 v51, v51, v53
	v_fmac_f32_e32 v19, v132, v132
	v_fmac_f32_e32 v20, v134, v134
	v_add_f32_e32 v14, v14, v15
	v_mul_f32_e32 v15, v123, v123
	v_mul_f32_e32 v16, v121, v121
	v_add_f32_e32 v49, v49, v51
	v_add_f32_e32 v19, v19, v20
	v_fmac_f32_e32 v15, v122, v122
	v_fmac_f32_e32 v16, v120, v120
	s_waitcnt vmcnt(5)
	v_and_b32_e32 v117, 0xffff0000, v12
	v_and_b32_e32 v115, 0xffff0000, v13
	v_add_f32_e32 v18, v47, v18
	v_add_f32_e32 v19, v49, v19
	v_add_f32_e32 v15, v15, v16
	v_lshlrev_b32_e32 v116, 16, v12
	v_lshlrev_b32_e32 v114, 16, v13
	s_waitcnt vmcnt(4)
	v_lshlrev_b32_e32 v112, 16, v10
	v_and_b32_e32 v113, 0xffff0000, v10
	v_lshlrev_b32_e32 v110, 16, v11
	v_and_b32_e32 v111, 0xffff0000, v11
	v_mul_f32_e32 v10, v117, v117
	v_mul_f32_e32 v11, v115, v115
	s_waitcnt vmcnt(3)
	v_and_b32_e32 v109, 0xffff0000, v8
	v_and_b32_e32 v107, 0xffff0000, v9
	v_add_f32_e32 v14, v18, v14
	v_add_f32_e32 v15, v19, v15
	v_fmac_f32_e32 v10, v116, v116
	v_fmac_f32_e32 v11, v114, v114
	v_lshlrev_b32_e32 v108, 16, v8
	v_lshlrev_b32_e32 v106, 16, v9
	s_waitcnt vmcnt(2)
	v_lshlrev_b32_e32 v20, 16, v6
	v_and_b32_e32 v21, 0xffff0000, v6
	v_lshlrev_b32_e32 v18, 16, v7
	v_and_b32_e32 v19, 0xffff0000, v7
	v_mul_f32_e32 v6, v109, v109
	v_mul_f32_e32 v7, v107, v107
	s_waitcnt vmcnt(1)
	v_and_b32_e32 v101, 0xffff0000, v2
	v_and_b32_e32 v99, 0xffff0000, v3
	v_add_f32_e32 v10, v10, v11
	v_fmac_f32_e32 v6, v108, v108
	v_fmac_f32_e32 v7, v106, v106
	v_lshlrev_b32_e32 v100, 16, v2
	v_lshlrev_b32_e32 v98, 16, v3
	v_mul_f32_e32 v2, v101, v101
	v_mul_f32_e32 v3, v99, v99
	v_add_f32_e32 v10, v14, v10
	v_add_f32_e32 v6, v6, v7
	s_waitcnt vmcnt(0)
	v_and_b32_e32 v97, 0xffff0000, v4
	v_and_b32_e32 v95, 0xffff0000, v5
	v_fmac_f32_e32 v2, v100, v100
	v_fmac_f32_e32 v3, v98, v98
	v_add_f32_e32 v6, v10, v6
	v_lshlrev_b32_e32 v96, 16, v4
	v_lshlrev_b32_e32 v94, 16, v5
	v_add_f32_e32 v2, v2, v3
	v_mul_f32_e32 v3, v97, v97
	v_mul_f32_e32 v4, v95, v95
	v_add_f32_e32 v2, v6, v2
	v_fmac_f32_e32 v3, v96, v96
	v_fmac_f32_e32 v4, v94, v94
	v_add_f32_e32 v3, v3, v4
	v_mov_b32_dpp v4, v2 quad_perm:[1,0,3,2] row_mask:0xf bank_mask:0xf
	v_mul_f32_e32 v11, v113, v113
	v_mul_f32_e32 v12, v111, v111
	v_fmac_f32_e32 v11, v112, v112
	v_fmac_f32_e32 v12, v110, v110
	s_waitcnt lgkmcnt(0)
	v_add_f32_e32 v2, v2, v4
	s_nop 1
	v_mov_b32_dpp v4, v2 quad_perm:[2,3,0,1] row_mask:0xf bank_mask:0xf
	v_mul_f32_e32 v7, v21, v21
	v_mul_f32_e32 v8, v19, v19
	v_add_f32_e32 v11, v11, v12
	v_fmac_f32_e32 v7, v20, v20
	s_waitcnt lgkmcnt(0)
	v_add_f32_e32 v2, v2, v4
	s_nop 1
	v_mov_b32_dpp v4, v2 row_half_mirror row_mask:0xf bank_mask:0xf
	v_fmac_f32_e32 v8, v18, v18
	v_add_f32_e32 v11, v15, v11
	v_add_f32_e32 v7, v7, v8
	v_add_f32_e32 v7, v11, v7
	s_waitcnt lgkmcnt(0)
	v_add_f32_e32 v2, v2, v4
	s_nop 1
	v_mov_b32_dpp v4, v2 row_mirror row_mask:0xf bank_mask:0xf
	v_add_f32_e32 v3, v7, v3
	v_mov_b32_e32 v51, 0
	s_waitcnt lgkmcnt(0)
	v_add_f32_e32 v2, v2, v4
	v_mov_b32_e32 v4, v2
	s_nop 1
	v_permlane16_swap_b32_e32 v2, v4
	v_add_f32_e32 v2, v2, v4
	v_mov_b32_e32 v4, v2
	s_nop 1
	v_permlane32_swap_b32_e32 v2, v4
	v_add_f32_e32 v2, v2, v4
	v_fmamk_f32 v2, v2, 0x3a000000, v228
	v_cmp_gt_f32_e32 vcc, s82, v2
	v_mul_f32_e32 v4, 0x4f800000, v2
	s_nop 0
	v_cndmask_b32_e32 v2, v2, v4, vcc
	v_sqrt_f32_e32 v4, v2
	s_nop 0
	v_add_u32_e32 v5, -1, v4
	v_fma_f32 v6, -v5, v4, v2
	v_cmp_ge_f32_e64 s[44:45], 0, v6
	v_add_u32_e32 v6, 1, v4
	s_nop 0
	v_cndmask_b32_e64 v5, v4, v5, s[44:45]
	v_fma_f32 v4, -v6, v4, v2
	v_cmp_lt_f32_e64 s[44:45], 0, v4
	s_nop 1
	v_cndmask_b32_e64 v4, v5, v6, s[44:45]
	v_mul_f32_e32 v5, 0x37800000, v4
	v_cndmask_b32_e32 v4, v4, v5, vcc
	v_cmp_class_f32_e32 vcc, v2, v229
	s_nop 1
	v_cndmask_b32_e32 v2, v4, v2, vcc
	v_mov_b32_dpp v4, v3 quad_perm:[1,0,3,2] row_mask:0xf bank_mask:0xf
	s_waitcnt lgkmcnt(0)
	v_add_f32_e32 v3, v3, v4
	s_nop 1
	v_mov_b32_dpp v4, v3 quad_perm:[2,3,0,1] row_mask:0xf bank_mask:0xf
	s_waitcnt lgkmcnt(0)
	v_add_f32_e32 v3, v3, v4
	s_nop 1
	v_mov_b32_dpp v4, v3 row_half_mirror row_mask:0xf bank_mask:0xf
	s_waitcnt lgkmcnt(0)
	v_add_f32_e32 v3, v3, v4
	s_nop 1
	v_mov_b32_dpp v4, v3 row_mirror row_mask:0xf bank_mask:0xf
	s_waitcnt lgkmcnt(0)
	v_add_f32_e32 v3, v3, v4
	v_mov_b32_e32 v4, v3
	s_nop 1
	v_permlane16_swap_b32_e32 v3, v4
	v_add_f32_e32 v3, v3, v4
	v_mov_b32_e32 v4, v3
	s_nop 1
	v_permlane32_swap_b32_e32 v3, v4
	v_add_f32_e32 v3, v3, v4
	v_fmamk_f32 v3, v3, 0x3a000000, v228
	v_cmp_gt_f32_e32 vcc, s82, v3
	v_mul_f32_e32 v4, 0x4f800000, v3
	s_nop 0
	v_cndmask_b32_e32 v3, v3, v4, vcc
	v_sqrt_f32_e32 v4, v3
	s_nop 0
	v_add_u32_e32 v5, -1, v4
	v_fma_f32 v6, -v5, v4, v3
	v_cmp_ge_f32_e64 s[44:45], 0, v6
	v_add_u32_e32 v6, 1, v4
	s_nop 0
	v_cndmask_b32_e64 v5, v4, v5, s[44:45]
	v_fma_f32 v4, -v6, v4, v3
	v_cmp_lt_f32_e64 s[44:45], 0, v4
	s_nop 1
	v_cndmask_b32_e64 v4, v5, v6, s[44:45]
	v_mul_f32_e32 v5, 0x37800000, v4
	v_cndmask_b32_e32 v4, v4, v5, vcc
	v_cmp_class_f32_e32 vcc, v3, v229
	s_nop 1
	v_cndmask_b32_e32 v3, v4, v3, vcc
	v_div_scale_f32 v4, s[4:5], v2, v2, 1.0
	v_rcp_f32_e32 v5, v4
	s_nop 0
	v_fma_f32 v6, -v4, v5, 1.0
	v_fmac_f32_e32 v5, v6, v5
	v_div_scale_f32 v6, vcc, 1.0, v2, 1.0
	v_mul_f32_e32 v7, v6, v5
	v_fma_f32 v8, -v4, v7, v6
	v_fmac_f32_e32 v7, v8, v5
	v_fma_f32 v4, -v4, v7, v6
	v_div_fmas_f32 v4, v4, v5, v7
	v_div_fixup_f32 v102, v4, v2, 1.0
	v_div_scale_f32 v2, s[4:5], v3, v3, 1.0
	v_rcp_f32_e32 v4, v2
	v_pk_mul_f32 v[156:157], v[102:103], v[156:157] op_sel_hi:[0,1]
	v_pk_mul_f32 v[154:155], v[102:103], v[154:155] op_sel_hi:[0,1]
	v_fma_f32 v5, -v2, v4, 1.0
	v_fmac_f32_e32 v4, v5, v4
	v_div_scale_f32 v5, vcc, 1.0, v3, 1.0
	v_mul_f32_e32 v6, v5, v4
	v_fma_f32 v7, -v2, v6, v5
	v_fmac_f32_e32 v6, v7, v4
	v_fma_f32 v2, -v2, v6, v5
	v_div_fmas_f32 v2, v2, v4, v6
	v_div_fixup_f32 v104, v2, v3, 1.0
	global_load_dwordx4 v[2:5], v[26:27], off
	global_load_dwordx4 v[6:9], v[62:63], off
	global_load_dwordx4 v[14:17], v[64:65], off
	v_pk_mul_f32 v[152:153], v[104:105], v[152:153] op_sel_hi:[0,1]
	v_pk_mul_f32 v[118:119], v[104:105], v[118:119] op_sel_hi:[0,1]
	s_waitcnt vmcnt(1)
	v_pk_add_f32 v[8:9], v[8:9], 1.0 op_sel_hi:[1,0]
	v_pk_add_f32 v[6:7], v[6:7], 1.0 op_sel_hi:[1,0]
	v_pk_mul_f32 v[160:161], v[4:5], v[8:9]
	v_pk_mul_f32 v[162:163], v[2:3], v[6:7]
	global_load_dwordx4 v[2:5], v[66:67], off
	global_load_dwordx4 v[10:13], v[68:69], off
	global_load_dwordx4 v[6:9], v[28:29], off
	s_waitcnt vmcnt(3)
	v_pk_fma_f32 v[156:157], v[162:163], v[156:157], v[14:15]
	v_pk_fma_f32 v[154:155], v[160:161], v[154:155], v[16:17]
	v_med3_f32 v47, v156, s33, v233
	v_med3_f32 v49, v157, s33, v233
	v_cvt_pk_fp8_f32 v51, v47, v49
	ds_read_b128 v[206:209], v105
	ds_read_b128 v[238:241], v105 offset:2048
	v_med3_f32 v47, v154, s33, v233
	v_med3_f32 v49, v155, s33, v233
	v_cvt_pk_fp8_f32 v51, v47, v49 op_sel:[0,0,1]
	v_pk_fma_f32 v[16:17], v[160:161], v[118:119], v[16:17]
	v_pk_fma_f32 v[14:15], v[162:163], v[152:153], v[14:15]
	v_add_co_u32_e32 v118, vcc, s80, v158
	s_waitcnt lgkmcnt(1)
	v_fma_f32 v224, v156, v206, 0
	v_addc_co_u32_e32 v119, vcc, 0, v159, vcc
	v_fma_f32 v223, v156, v207, 0
	v_fma_f32 v221, v156, v208, 0
	v_fma_f32 v217, v156, v209, 0
	v_fma_f32 v225, v14, v206, 0
	v_fma_f32 v222, v14, v207, 0
	v_fma_f32 v219, v14, v208, 0
	v_fma_f32 v215, v14, v209, 0
	ds_read_b128 v[206:209], v105 offset:1024
	global_store_dword v[118:119], v51, off
	v_med3_f32 v47, v14, s33, v233
	v_med3_f32 v49, v15, s33, v233
	v_mov_b32_e32 v51, 0
	v_cvt_pk_fp8_f32 v51, v47, v49
	v_med3_f32 v47, v16, s33, v233
	v_med3_f32 v49, v17, s33, v233
	s_waitcnt lgkmcnt(0)
	v_fma_f32 v220, v156, v206, 0
	v_fma_f32 v216, v156, v207, 0
	v_fma_f32 v213, v156, v208, 0
	v_fma_f32 v211, v156, v209, 0
	v_fma_f32 v218, v14, v206, 0
	v_fma_f32 v214, v14, v207, 0
	v_fma_f32 v212, v14, v208, 0
	v_fma_f32 v210, v14, v209, 0
	v_fma_f32 v209, v156, v238, 0
	v_fma_f32 v207, v156, v239, 0
	v_fma_f32 v205, v156, v240, 0
	v_fma_f32 v153, v156, v241, 0
	v_fma_f32 v208, v14, v238, 0
	v_fma_f32 v206, v14, v239, 0
	v_fma_f32 v158, v14, v240, 0
	v_fma_f32 v57, v14, v241, 0
	ds_read_b128 v[238:241], v105 offset:3072
	v_cvt_pk_fp8_f32 v51, v47, v49 op_sel:[0,0,1]
	global_store_dword v[118:119], v51, off offset:2048
	s_waitcnt lgkmcnt(0)
	v_fma_f32 v159, v156, v238, 0
	v_fma_f32 v152, v156, v239, 0
	v_fma_f32 v53, v156, v240, 0
	v_fma_f32 v49, v156, v241, 0
	v_fma_f32 v156, v14, v238, 0
	v_fma_f32 v55, v14, v239, 0
	v_fma_f32 v51, v14, v240, 0
	v_fma_f32 v47, v14, v241, 0
	ds_read_b128 v[234:237], v105 offset:4096
	ds_read_b128 v[242:245], v105 offset:5120
	ds_read_b128 v[246:249], v105 offset:6144
	s_waitcnt lgkmcnt(2)
	v_fmac_f32_e32 v224, v157, v234
	v_fmac_f32_e32 v223, v157, v235
	v_fmac_f32_e32 v221, v157, v236
	v_fmac_f32_e32 v217, v157, v237
	v_fmac_f32_e32 v225, v15, v234
	v_fmac_f32_e32 v222, v15, v235
	v_fmac_f32_e32 v219, v15, v236
	v_fmac_f32_e32 v215, v15, v237
	ds_read_b128 v[234:237], v105 offset:7168
	s_waitcnt lgkmcnt(2)
	v_fmac_f32_e32 v220, v157, v242
	v_fmac_f32_e32 v216, v157, v243
	v_fmac_f32_e32 v213, v157, v244
	v_fmac_f32_e32 v211, v157, v245
	v_fmac_f32_e32 v218, v15, v242
	v_fmac_f32_e32 v214, v15, v243
	v_fmac_f32_e32 v212, v15, v244
	v_fmac_f32_e32 v210, v15, v245
	ds_read_b128 v[242:245], v105 offset:8192
	s_waitcnt lgkmcnt(2)
	v_fmac_f32_e32 v209, v157, v246
	v_fmac_f32_e32 v207, v157, v247
	v_fmac_f32_e32 v205, v157, v248
	v_fmac_f32_e32 v153, v157, v249
	v_fmac_f32_e32 v208, v15, v246
	v_fmac_f32_e32 v206, v15, v247
	v_fmac_f32_e32 v158, v15, v248
	v_fmac_f32_e32 v57, v15, v249
	ds_read_b128 v[246:249], v105 offset:9216
	s_waitcnt lgkmcnt(2)
	v_fmac_f32_e32 v159, v157, v234
	v_fmac_f32_e32 v152, v157, v235
	v_fmac_f32_e32 v53, v157, v236
	v_fmac_f32_e32 v49, v157, v237
	v_fmac_f32_e32 v156, v15, v234
	v_fmac_f32_e32 v55, v15, v235
	v_fmac_f32_e32 v51, v15, v236
	v_fmac_f32_e32 v47, v15, v237
	ds_read_b128 v[234:237], v105 offset:10240
	s_waitcnt lgkmcnt(2)
	v_fmac_f32_e32 v224, v154, v242
	v_fmac_f32_e32 v223, v154, v243
	v_fmac_f32_e32 v221, v154, v244
	v_fmac_f32_e32 v217, v154, v245
	v_fmac_f32_e32 v225, v16, v242
	v_fmac_f32_e32 v222, v16, v243
	v_fmac_f32_e32 v219, v16, v244
	v_fmac_f32_e32 v215, v16, v245
	ds_read_b128 v[242:245], v105 offset:11264
	s_waitcnt lgkmcnt(2)
	v_fmac_f32_e32 v220, v154, v246
	v_fmac_f32_e32 v216, v154, v247
	v_fmac_f32_e32 v213, v154, v248
	v_fmac_f32_e32 v211, v154, v249
	v_fmac_f32_e32 v218, v16, v246
	v_fmac_f32_e32 v214, v16, v247
	v_fmac_f32_e32 v212, v16, v248
	v_fmac_f32_e32 v210, v16, v249
	ds_read_b128 v[246:249], v105 offset:12288
	s_waitcnt lgkmcnt(2)
	v_fmac_f32_e32 v209, v154, v234
	v_fmac_f32_e32 v207, v154, v235
	v_fmac_f32_e32 v205, v154, v236
	v_fmac_f32_e32 v153, v154, v237
	v_fmac_f32_e32 v208, v16, v234
	v_fmac_f32_e32 v206, v16, v235
	v_fmac_f32_e32 v158, v16, v236
	v_fmac_f32_e32 v57, v16, v237
	ds_read_b128 v[234:237], v105 offset:13312
	s_waitcnt lgkmcnt(2)
	v_fmac_f32_e32 v159, v154, v242
	v_fmac_f32_e32 v152, v154, v243
	v_fmac_f32_e32 v53, v154, v244
	v_fmac_f32_e32 v49, v154, v245
	v_fmac_f32_e32 v156, v16, v242
	v_fmac_f32_e32 v55, v16, v243
	v_fmac_f32_e32 v51, v16, v244
	v_fmac_f32_e32 v47, v16, v245
	ds_read_b128 v[242:245], v105 offset:14336
	s_waitcnt lgkmcnt(2)
	v_fmac_f32_e32 v224, v155, v246
	v_fmac_f32_e32 v223, v155, v247
	v_fmac_f32_e32 v221, v155, v248
	v_fmac_f32_e32 v217, v155, v249
	v_fmac_f32_e32 v225, v17, v246
	v_fmac_f32_e32 v222, v17, v247
	v_fmac_f32_e32 v219, v17, v248
	v_fmac_f32_e32 v215, v17, v249
	ds_read_b128 v[246:249], v105 offset:15360
	s_waitcnt lgkmcnt(2)
	v_fmac_f32_e32 v220, v155, v234
	v_fmac_f32_e32 v216, v155, v235
	v_fmac_f32_e32 v213, v155, v236
	v_fmac_f32_e32 v211, v155, v237
	v_fmac_f32_e32 v218, v17, v234
	v_fmac_f32_e32 v214, v17, v235
	v_fmac_f32_e32 v212, v17, v236
	v_fmac_f32_e32 v210, v17, v237
	ds_read_b128 v[234:237], v105 offset:16384
	s_waitcnt lgkmcnt(2)
	v_fmac_f32_e32 v209, v155, v242
	v_fmac_f32_e32 v207, v155, v243
	v_fmac_f32_e32 v205, v155, v244
	v_fmac_f32_e32 v153, v155, v245
	v_fmac_f32_e32 v208, v17, v242
	v_fmac_f32_e32 v206, v17, v243
	v_fmac_f32_e32 v158, v17, v244
	v_fmac_f32_e32 v57, v17, v245
	ds_read_b128 v[242:245], v105 offset:17408
	s_waitcnt lgkmcnt(2)
	v_fmac_f32_e32 v53, v155, v248
	v_fmac_f32_e32 v55, v17, v247
	v_fmac_f32_e32 v51, v17, v248
	v_fmac_f32_e32 v159, v155, v246
	v_fmac_f32_e32 v152, v155, v247
	v_fmac_f32_e32 v49, v155, v249
	v_fmac_f32_e32 v156, v17, v246
	v_fmac_f32_e32 v47, v17, v249
	ds_read_b128 v[246:249], v105 offset:18432
	s_waitcnt vmcnt(3)
	v_pk_add_f32 v[10:11], v[10:11], 1.0 op_sel_hi:[1,0]
	v_pk_mul_f32 v[150:151], v[102:103], v[150:151] op_sel_hi:[0,1]
	s_waitcnt vmcnt(2)
	v_pk_mul_f32 v[154:155], v[6:7], v[10:11]
	v_pk_add_f32 v[12:13], v[12:13], 1.0 op_sel_hi:[1,0]
	v_pk_fma_f32 v[160:161], v[150:151], v[154:155], v[2:3]
	v_pk_mul_f32 v[146:147], v[104:105], v[146:147] op_sel_hi:[0,1]
	v_pk_mul_f32 v[16:17], v[8:9], v[12:13]
	v_pk_mul_f32 v[14:15], v[102:103], v[148:149] op_sel_hi:[0,1]
	v_pk_mul_f32 v[144:145], v[104:105], v[144:145] op_sel_hi:[0,1]
	v_pk_fma_f32 v[154:155], v[154:155], v[146:147], v[2:3]
	v_med3_f32 v2, v160, s33, v233
	v_med3_f32 v3, v161, s33, v233
	v_mov_b32_e32 v148, 0
	v_pk_fma_f32 v[14:15], v[14:15], v[16:17], v[4:5]
	v_pk_fma_f32 v[16:17], v[16:17], v[144:145], v[4:5]
	v_cvt_pk_fp8_f32 v148, v2, v3
	v_med3_f32 v4, v154, s33, v233
	v_med3_f32 v5, v155, s33, v233
	v_mov_b32_e32 v149, 0
	v_cvt_pk_fp8_f32 v149, v4, v5
	v_med3_f32 v2, v14, s33, v233
	v_med3_f32 v3, v15, s33, v233
	v_cvt_pk_fp8_f32 v148, v2, v3 op_sel:[0,0,1]
	v_med3_f32 v2, v16, s33, v233
	v_med3_f32 v3, v17, s33, v233
	global_load_dwordx4 v[6:9], v[70:71], off
	global_load_dwordx4 v[10:13], v[72:73], off
	v_cvt_pk_fp8_f32 v149, v2, v3 op_sel:[0,0,1]
	global_load_dwordx4 v[2:5], v[30:31], off
	global_store_dword v[118:119], v148, off offset:256
	global_store_dword v[118:119], v149, off offset:2304
	s_waitcnt lgkmcnt(2)
	v_fmac_f32_e32 v224, v160, v234
	v_fmac_f32_e32 v223, v160, v235
	v_fmac_f32_e32 v221, v160, v236
	v_fmac_f32_e32 v217, v160, v237
	v_fmac_f32_e32 v225, v154, v234
	v_fmac_f32_e32 v222, v154, v235
	v_fmac_f32_e32 v219, v154, v236
	v_fmac_f32_e32 v215, v154, v237
	ds_read_b128 v[234:237], v105 offset:19456
	s_waitcnt lgkmcnt(2)
	v_fmac_f32_e32 v220, v160, v242
	v_fmac_f32_e32 v216, v160, v243
	v_fmac_f32_e32 v213, v160, v244
	v_fmac_f32_e32 v211, v160, v245
	v_fmac_f32_e32 v218, v154, v242
	v_fmac_f32_e32 v214, v154, v243
	v_fmac_f32_e32 v212, v154, v244
	v_fmac_f32_e32 v210, v154, v245
	ds_read_b128 v[242:245], v105 offset:20480
	s_waitcnt lgkmcnt(2)
	v_fmac_f32_e32 v209, v160, v246
	v_fmac_f32_e32 v207, v160, v247
	v_fmac_f32_e32 v205, v160, v248
	v_fmac_f32_e32 v153, v160, v249
	v_fmac_f32_e32 v208, v154, v246
	v_fmac_f32_e32 v206, v154, v247
	v_fmac_f32_e32 v158, v154, v248
	v_fmac_f32_e32 v57, v154, v249
	ds_read_b128 v[246:249], v105 offset:21504
	s_waitcnt lgkmcnt(2)
	v_fmac_f32_e32 v159, v160, v234
	v_fmac_f32_e32 v152, v160, v235
	v_fmac_f32_e32 v53, v160, v236
	v_fmac_f32_e32 v49, v160, v237
	v_fmac_f32_e32 v156, v154, v234
	v_fmac_f32_e32 v55, v154, v235
	v_fmac_f32_e32 v51, v154, v236
	v_fmac_f32_e32 v47, v154, v237
	ds_read_b128 v[234:237], v105 offset:22528
	s_waitcnt lgkmcnt(2)
	v_fmac_f32_e32 v224, v161, v242
	v_fmac_f32_e32 v223, v161, v243
	v_fmac_f32_e32 v221, v161, v244
	v_fmac_f32_e32 v217, v161, v245
	v_fmac_f32_e32 v225, v155, v242
	v_fmac_f32_e32 v222, v155, v243
	v_fmac_f32_e32 v219, v155, v244
	v_fmac_f32_e32 v215, v155, v245
	ds_read_b128 v[242:245], v105 offset:23552
	s_waitcnt lgkmcnt(2)
	v_fmac_f32_e32 v220, v161, v246
	v_fmac_f32_e32 v216, v161, v247
	v_fmac_f32_e32 v213, v161, v248
	v_fmac_f32_e32 v211, v161, v249
	v_fmac_f32_e32 v218, v155, v246
	v_fmac_f32_e32 v214, v155, v247
	v_fmac_f32_e32 v212, v155, v248
	v_fmac_f32_e32 v210, v155, v249
	ds_read_b128 v[246:249], v105 offset:24576
	s_waitcnt lgkmcnt(2)
	v_fmac_f32_e32 v209, v161, v234
	v_fmac_f32_e32 v207, v161, v235
	v_fmac_f32_e32 v205, v161, v236
	v_fmac_f32_e32 v153, v161, v237
	v_fmac_f32_e32 v208, v155, v234
	v_fmac_f32_e32 v206, v155, v235
	v_fmac_f32_e32 v158, v155, v236
	v_fmac_f32_e32 v57, v155, v237
	ds_read_b128 v[234:237], v105 offset:25600
	s_waitcnt lgkmcnt(2)
	v_fmac_f32_e32 v159, v161, v242
	v_fmac_f32_e32 v152, v161, v243
	v_fmac_f32_e32 v53, v161, v244
	v_fmac_f32_e32 v49, v161, v245
	v_fmac_f32_e32 v156, v155, v242
	v_fmac_f32_e32 v55, v155, v243
	v_fmac_f32_e32 v51, v155, v244
	v_fmac_f32_e32 v47, v155, v245
	ds_read_b128 v[242:245], v105 offset:26624
	s_waitcnt lgkmcnt(2)
	v_fmac_f32_e32 v224, v14, v246
	v_fmac_f32_e32 v223, v14, v247
	v_fmac_f32_e32 v221, v14, v248
	v_fmac_f32_e32 v217, v14, v249
	v_fmac_f32_e32 v225, v16, v246
	v_fmac_f32_e32 v222, v16, v247
	v_fmac_f32_e32 v219, v16, v248
	v_fmac_f32_e32 v215, v16, v249
	ds_read_b128 v[246:249], v105 offset:27648
	s_waitcnt lgkmcnt(2)
	v_fmac_f32_e32 v220, v14, v234
	v_fmac_f32_e32 v216, v14, v235
	v_fmac_f32_e32 v213, v14, v236
	v_fmac_f32_e32 v211, v14, v237
	v_fmac_f32_e32 v218, v16, v234
	v_fmac_f32_e32 v214, v16, v235
	v_fmac_f32_e32 v212, v16, v236
	v_fmac_f32_e32 v210, v16, v237
	ds_read_b128 v[234:237], v105 offset:28672
	s_waitcnt lgkmcnt(2)
	v_fmac_f32_e32 v209, v14, v242
	v_fmac_f32_e32 v207, v14, v243
	v_fmac_f32_e32 v205, v14, v244
	v_fmac_f32_e32 v153, v14, v245
	v_fmac_f32_e32 v208, v16, v242
	v_fmac_f32_e32 v206, v16, v243
	v_fmac_f32_e32 v158, v16, v244
	v_fmac_f32_e32 v57, v16, v245
	ds_read_b128 v[242:245], v105 offset:29696
	s_waitcnt lgkmcnt(2)
	v_fmac_f32_e32 v159, v14, v246
	v_fmac_f32_e32 v152, v14, v247
	v_fmac_f32_e32 v53, v14, v248
	v_fmac_f32_e32 v49, v14, v249
	v_fmac_f32_e32 v156, v16, v246
	v_fmac_f32_e32 v55, v16, v247
	v_fmac_f32_e32 v51, v16, v248
	v_fmac_f32_e32 v47, v16, v249
	ds_read_b128 v[246:249], v105 offset:30720
	s_waitcnt lgkmcnt(2)
	v_fmac_f32_e32 v224, v15, v234
	v_fmac_f32_e32 v223, v15, v235
	v_fmac_f32_e32 v221, v15, v236
	v_fmac_f32_e32 v217, v15, v237
	v_fmac_f32_e32 v225, v17, v234
	v_fmac_f32_e32 v222, v17, v235
	v_fmac_f32_e32 v219, v17, v236
	v_fmac_f32_e32 v215, v17, v237
	ds_read_b128 v[234:237], v105 offset:31744
	s_waitcnt lgkmcnt(2)
	v_fmac_f32_e32 v220, v15, v242
	v_fmac_f32_e32 v216, v15, v243
	v_fmac_f32_e32 v213, v15, v244
	v_fmac_f32_e32 v211, v15, v245
	v_fmac_f32_e32 v218, v17, v242
	v_fmac_f32_e32 v214, v17, v243
	v_fmac_f32_e32 v212, v17, v244
	v_fmac_f32_e32 v210, v17, v245
	ds_read_b128 v[242:245], v105 offset:32768
	s_waitcnt lgkmcnt(2)
	v_fmac_f32_e32 v57, v17, v249
	v_fmac_f32_e32 v209, v15, v246
	v_fmac_f32_e32 v207, v15, v247
	v_fmac_f32_e32 v205, v15, v248
	s_waitcnt lgkmcnt(1)
	v_fmac_f32_e32 v53, v15, v236
	v_fmac_f32_e32 v55, v17, v235
	v_fmac_f32_e32 v51, v17, v236
	v_fmac_f32_e32 v153, v15, v249
	v_fmac_f32_e32 v208, v17, v246
	v_fmac_f32_e32 v206, v17, v247
	v_fmac_f32_e32 v158, v17, v248
	ds_read_b128 v[246:249], v105 offset:33792
	v_fmac_f32_e32 v159, v15, v234
	v_fmac_f32_e32 v152, v15, v235
	v_fmac_f32_e32 v49, v15, v237
	v_fmac_f32_e32 v156, v17, v234
	v_fmac_f32_e32 v47, v17, v237
	ds_read_b128 v[234:237], v105 offset:34816
	s_waitcnt vmcnt(3)
	v_pk_add_f32 v[10:11], v[10:11], 1.0 op_sel_hi:[1,0]
	v_pk_mul_f32 v[142:143], v[102:103], v[142:143] op_sel_hi:[0,1]
	s_waitcnt vmcnt(2)
	v_pk_mul_f32 v[144:145], v[2:3], v[10:11]
	v_pk_add_f32 v[12:13], v[12:13], 1.0 op_sel_hi:[1,0]
	v_pk_fma_f32 v[146:147], v[142:143], v[144:145], v[6:7]
	v_pk_mul_f32 v[138:139], v[104:105], v[138:139] op_sel_hi:[0,1]
	v_pk_mul_f32 v[16:17], v[4:5], v[12:13]
	v_pk_mul_f32 v[14:15], v[102:103], v[140:141] op_sel_hi:[0,1]
	v_pk_mul_f32 v[136:137], v[104:105], v[136:137] op_sel_hi:[0,1]
	v_pk_fma_f32 v[144:145], v[138:139], v[144:145], v[6:7]
	v_med3_f32 v6, v146, s33, v233
	v_med3_f32 v7, v147, s33, v233
	v_mov_b32_e32 v140, 0
	v_pk_fma_f32 v[14:15], v[14:15], v[16:17], v[8:9]
	v_pk_fma_f32 v[16:17], v[136:137], v[16:17], v[8:9]
	v_cvt_pk_fp8_f32 v140, v6, v7
	v_med3_f32 v8, v144, s33, v233
	v_med3_f32 v9, v145, s33, v233
	v_mov_b32_e32 v141, 0
	v_cvt_pk_fp8_f32 v141, v8, v9
	v_med3_f32 v6, v14, s33, v233
	v_med3_f32 v7, v15, s33, v233
	v_cvt_pk_fp8_f32 v140, v6, v7 op_sel:[0,0,1]
	v_med3_f32 v6, v16, s33, v233
	v_med3_f32 v7, v17, s33, v233
	global_load_dwordx4 v[2:5], v[74:75], off
	global_load_dwordx4 v[10:13], v[76:77], off
	v_cvt_pk_fp8_f32 v141, v6, v7 op_sel:[0,0,1]
	global_load_dwordx4 v[6:9], v[32:33], off
	global_store_dword v[118:119], v140, off offset:512
	global_store_dword v[118:119], v141, off offset:2560
	s_waitcnt lgkmcnt(2)
	v_fmac_f32_e32 v224, v146, v242
	v_fmac_f32_e32 v223, v146, v243
	v_fmac_f32_e32 v221, v146, v244
	v_fmac_f32_e32 v217, v146, v245
	v_fmac_f32_e32 v225, v144, v242
	v_fmac_f32_e32 v222, v144, v243
	v_fmac_f32_e32 v219, v144, v244
	v_fmac_f32_e32 v215, v144, v245
	ds_read_b128 v[242:245], v105 offset:35840
	s_waitcnt lgkmcnt(2)
	v_fmac_f32_e32 v220, v146, v246
	v_fmac_f32_e32 v216, v146, v247
	v_fmac_f32_e32 v213, v146, v248
	v_fmac_f32_e32 v211, v146, v249
	v_fmac_f32_e32 v218, v144, v246
	v_fmac_f32_e32 v214, v144, v247
	v_fmac_f32_e32 v212, v144, v248
	v_fmac_f32_e32 v210, v144, v249
	ds_read_b128 v[246:249], v105 offset:36864
	s_waitcnt lgkmcnt(2)
	v_fmac_f32_e32 v209, v146, v234
	v_fmac_f32_e32 v207, v146, v235
	v_fmac_f32_e32 v205, v146, v236
	v_fmac_f32_e32 v153, v146, v237
	v_fmac_f32_e32 v208, v144, v234
	v_fmac_f32_e32 v206, v144, v235
	v_fmac_f32_e32 v158, v144, v236
	v_fmac_f32_e32 v57, v144, v237
	ds_read_b128 v[234:237], v105 offset:37888
	s_waitcnt lgkmcnt(2)
	v_fmac_f32_e32 v159, v146, v242
	v_fmac_f32_e32 v152, v146, v243
	v_fmac_f32_e32 v53, v146, v244
	v_fmac_f32_e32 v49, v146, v245
	v_fmac_f32_e32 v156, v144, v242
	v_fmac_f32_e32 v55, v144, v243
	v_fmac_f32_e32 v51, v144, v244
	v_fmac_f32_e32 v47, v144, v245
	ds_read_b128 v[242:245], v105 offset:38912
	s_waitcnt lgkmcnt(2)
	v_fmac_f32_e32 v224, v147, v246
	v_fmac_f32_e32 v223, v147, v247
	v_fmac_f32_e32 v221, v147, v248
	v_fmac_f32_e32 v217, v147, v249
	v_fmac_f32_e32 v225, v145, v246
	v_fmac_f32_e32 v222, v145, v247
	v_fmac_f32_e32 v219, v145, v248
	v_fmac_f32_e32 v215, v145, v249
	ds_read_b128 v[246:249], v105 offset:39936
	s_waitcnt lgkmcnt(2)
	v_fmac_f32_e32 v220, v147, v234
	v_fmac_f32_e32 v216, v147, v235
	v_fmac_f32_e32 v213, v147, v236
	v_fmac_f32_e32 v211, v147, v237
	v_fmac_f32_e32 v218, v145, v234
	v_fmac_f32_e32 v214, v145, v235
	v_fmac_f32_e32 v212, v145, v236
	v_fmac_f32_e32 v210, v145, v237
	ds_read_b128 v[234:237], v105 offset:40960
	s_waitcnt lgkmcnt(2)
	v_fmac_f32_e32 v209, v147, v242
	v_fmac_f32_e32 v207, v147, v243
	v_fmac_f32_e32 v205, v147, v244
	v_fmac_f32_e32 v153, v147, v245
	v_fmac_f32_e32 v208, v145, v242
	v_fmac_f32_e32 v206, v145, v243
	v_fmac_f32_e32 v158, v145, v244
	v_fmac_f32_e32 v57, v145, v245
	ds_read_b128 v[242:245], v105 offset:41984
	s_waitcnt lgkmcnt(2)
	v_fmac_f32_e32 v159, v147, v246
	v_fmac_f32_e32 v152, v147, v247
	v_fmac_f32_e32 v53, v147, v248
	v_fmac_f32_e32 v49, v147, v249
	v_fmac_f32_e32 v156, v145, v246
	v_fmac_f32_e32 v55, v145, v247
	v_fmac_f32_e32 v51, v145, v248
	v_fmac_f32_e32 v47, v145, v249
	ds_read_b128 v[246:249], v105 offset:43008
	s_waitcnt lgkmcnt(2)
	v_fmac_f32_e32 v224, v14, v234
	v_fmac_f32_e32 v223, v14, v235
	v_fmac_f32_e32 v221, v14, v236
	v_fmac_f32_e32 v217, v14, v237
	v_fmac_f32_e32 v225, v16, v234
	v_fmac_f32_e32 v222, v16, v235
	v_fmac_f32_e32 v219, v16, v236
	v_fmac_f32_e32 v215, v16, v237
	ds_read_b128 v[234:237], v105 offset:44032
	s_waitcnt lgkmcnt(2)
	v_fmac_f32_e32 v220, v14, v242
	v_fmac_f32_e32 v216, v14, v243
	v_fmac_f32_e32 v213, v14, v244
	v_fmac_f32_e32 v211, v14, v245
	v_fmac_f32_e32 v218, v16, v242
	v_fmac_f32_e32 v214, v16, v243
	v_fmac_f32_e32 v212, v16, v244
	v_fmac_f32_e32 v210, v16, v245
	ds_read_b128 v[242:245], v105 offset:45056
	s_waitcnt lgkmcnt(2)
	v_fmac_f32_e32 v209, v14, v246
	v_fmac_f32_e32 v207, v14, v247
	v_fmac_f32_e32 v205, v14, v248
	v_fmac_f32_e32 v153, v14, v249
	v_fmac_f32_e32 v208, v16, v246
	v_fmac_f32_e32 v206, v16, v247
	v_fmac_f32_e32 v158, v16, v248
	v_fmac_f32_e32 v57, v16, v249
	ds_read_b128 v[246:249], v105 offset:46080
	s_waitcnt lgkmcnt(2)
	v_fmac_f32_e32 v159, v14, v234
	v_fmac_f32_e32 v152, v14, v235
	v_fmac_f32_e32 v53, v14, v236
	v_fmac_f32_e32 v49, v14, v237
	v_fmac_f32_e32 v156, v16, v234
	v_fmac_f32_e32 v55, v16, v235
	v_fmac_f32_e32 v51, v16, v236
	v_fmac_f32_e32 v47, v16, v237
	ds_read_b128 v[234:237], v105 offset:47104
	s_waitcnt lgkmcnt(2)
	v_fmac_f32_e32 v224, v15, v242
	v_fmac_f32_e32 v223, v15, v243
	v_fmac_f32_e32 v221, v15, v244
	v_fmac_f32_e32 v217, v15, v245
	v_fmac_f32_e32 v225, v17, v242
	v_fmac_f32_e32 v222, v17, v243
	v_fmac_f32_e32 v219, v17, v244
	v_fmac_f32_e32 v215, v17, v245
	ds_read_b128 v[242:245], v105 offset:48128
	s_waitcnt lgkmcnt(2)
	v_fmac_f32_e32 v220, v15, v246
	v_fmac_f32_e32 v216, v15, v247
	v_fmac_f32_e32 v213, v15, v248
	v_fmac_f32_e32 v211, v15, v249
	v_fmac_f32_e32 v218, v17, v246
	v_fmac_f32_e32 v214, v17, v247
	v_fmac_f32_e32 v212, v17, v248
	v_fmac_f32_e32 v210, v17, v249
	ds_read_b128 v[246:249], v105 offset:49152
	s_waitcnt lgkmcnt(2)
	v_fmac_f32_e32 v57, v17, v237
	v_fmac_f32_e32 v209, v15, v234
	v_fmac_f32_e32 v207, v15, v235
	v_fmac_f32_e32 v205, v15, v236
	s_waitcnt lgkmcnt(1)
	v_fmac_f32_e32 v53, v15, v244
	v_fmac_f32_e32 v55, v17, v243
	v_fmac_f32_e32 v51, v17, v244
	v_fmac_f32_e32 v153, v15, v237
	v_fmac_f32_e32 v208, v17, v234
	v_fmac_f32_e32 v206, v17, v235
	v_fmac_f32_e32 v158, v17, v236
	ds_read_b128 v[234:237], v105 offset:50176
	v_fmac_f32_e32 v159, v15, v242
	v_fmac_f32_e32 v152, v15, v243
	v_fmac_f32_e32 v49, v15, v245
	v_fmac_f32_e32 v156, v17, v242
	v_fmac_f32_e32 v47, v17, v245
	ds_read_b128 v[242:245], v105 offset:51200
	s_waitcnt vmcnt(3)
	v_pk_add_f32 v[10:11], v[10:11], 1.0 op_sel_hi:[1,0]
	v_pk_mul_f32 v[130:131], v[102:103], v[130:131] op_sel_hi:[0,1]
	s_waitcnt vmcnt(2)
	v_pk_mul_f32 v[136:137], v[6:7], v[10:11]
	v_pk_add_f32 v[12:13], v[12:13], 1.0 op_sel_hi:[1,0]
	v_pk_mul_f32 v[14:15], v[102:103], v[128:129] op_sel_hi:[0,1]
	v_pk_fma_f32 v[138:139], v[130:131], v[136:137], v[2:3]
	v_pk_mul_f32 v[128:129], v[104:105], v[132:133] op_sel_hi:[0,1]
	v_pk_mul_f32 v[16:17], v[8:9], v[12:13]
	v_pk_mul_f32 v[130:131], v[104:105], v[134:135] op_sel_hi:[0,1]
	v_pk_fma_f32 v[136:137], v[128:129], v[136:137], v[2:3]
	v_med3_f32 v2, v138, s33, v233
	v_med3_f32 v3, v139, s33, v233
	v_mov_b32_e32 v132, 0
	v_pk_fma_f32 v[14:15], v[14:15], v[16:17], v[4:5]
	v_pk_fma_f32 v[16:17], v[130:131], v[16:17], v[4:5]
	v_cvt_pk_fp8_f32 v132, v2, v3
	v_med3_f32 v4, v136, s33, v233
	v_med3_f32 v5, v137, s33, v233
	v_mov_b32_e32 v133, 0
	v_cvt_pk_fp8_f32 v133, v4, v5
	v_med3_f32 v2, v14, s33, v233
	v_med3_f32 v3, v15, s33, v233
	v_cvt_pk_fp8_f32 v132, v2, v3 op_sel:[0,0,1]
	v_med3_f32 v2, v16, s33, v233
	v_med3_f32 v3, v17, s33, v233
	global_load_dwordx4 v[10:13], v[78:79], off
	global_load_dwordx4 v[6:9], v[80:81], off
	v_cvt_pk_fp8_f32 v133, v2, v3 op_sel:[0,0,1]
	global_load_dwordx4 v[2:5], v[34:35], off
	global_store_dword v[118:119], v132, off offset:768
	global_store_dword v[118:119], v133, off offset:2816
	s_waitcnt lgkmcnt(2)
	v_fmac_f32_e32 v224, v138, v246
	v_fmac_f32_e32 v223, v138, v247
	v_fmac_f32_e32 v221, v138, v248
	v_fmac_f32_e32 v217, v138, v249
	v_fmac_f32_e32 v225, v136, v246
	v_fmac_f32_e32 v222, v136, v247
	v_fmac_f32_e32 v219, v136, v248
	v_fmac_f32_e32 v215, v136, v249
	ds_read_b128 v[246:249], v105 offset:52224
	s_waitcnt lgkmcnt(2)
	v_fmac_f32_e32 v220, v138, v234
	v_fmac_f32_e32 v216, v138, v235
	v_fmac_f32_e32 v213, v138, v236
	v_fmac_f32_e32 v211, v138, v237
	v_fmac_f32_e32 v218, v136, v234
	v_fmac_f32_e32 v214, v136, v235
	v_fmac_f32_e32 v212, v136, v236
	v_fmac_f32_e32 v210, v136, v237
	ds_read_b128 v[234:237], v105 offset:53248
	s_waitcnt lgkmcnt(2)
	v_fmac_f32_e32 v209, v138, v242
	v_fmac_f32_e32 v207, v138, v243
	v_fmac_f32_e32 v205, v138, v244
	v_fmac_f32_e32 v153, v138, v245
	v_fmac_f32_e32 v208, v136, v242
	v_fmac_f32_e32 v206, v136, v243
	v_fmac_f32_e32 v158, v136, v244
	v_fmac_f32_e32 v57, v136, v245
	ds_read_b128 v[242:245], v105 offset:54272
	s_waitcnt lgkmcnt(2)
	v_fmac_f32_e32 v159, v138, v246
	v_fmac_f32_e32 v152, v138, v247
	v_fmac_f32_e32 v53, v138, v248
	v_fmac_f32_e32 v49, v138, v249
	v_fmac_f32_e32 v156, v136, v246
	v_fmac_f32_e32 v55, v136, v247
	v_fmac_f32_e32 v51, v136, v248
	v_fmac_f32_e32 v47, v136, v249
	ds_read_b128 v[246:249], v105 offset:55296
	s_waitcnt lgkmcnt(2)
	v_fmac_f32_e32 v224, v139, v234
	v_fmac_f32_e32 v223, v139, v235
	v_fmac_f32_e32 v221, v139, v236
	v_fmac_f32_e32 v217, v139, v237
	v_fmac_f32_e32 v225, v137, v234
	v_fmac_f32_e32 v222, v137, v235
	v_fmac_f32_e32 v219, v137, v236
	v_fmac_f32_e32 v215, v137, v237
	ds_read_b128 v[234:237], v105 offset:56320
	s_waitcnt lgkmcnt(2)
	v_fmac_f32_e32 v220, v139, v242
	v_fmac_f32_e32 v216, v139, v243
	v_fmac_f32_e32 v213, v139, v244
	v_fmac_f32_e32 v211, v139, v245
	v_fmac_f32_e32 v218, v137, v242
	v_fmac_f32_e32 v214, v137, v243
	v_fmac_f32_e32 v212, v137, v244
	v_fmac_f32_e32 v210, v137, v245
	ds_read_b128 v[242:245], v105 offset:57344
	s_waitcnt lgkmcnt(2)
	v_fmac_f32_e32 v209, v139, v246
	v_fmac_f32_e32 v207, v139, v247
	v_fmac_f32_e32 v205, v139, v248
	v_fmac_f32_e32 v153, v139, v249
	v_fmac_f32_e32 v208, v137, v246
	v_fmac_f32_e32 v206, v137, v247
	v_fmac_f32_e32 v158, v137, v248
	v_fmac_f32_e32 v57, v137, v249
	ds_read_b128 v[246:249], v105 offset:58368
	s_waitcnt lgkmcnt(2)
	v_fmac_f32_e32 v159, v139, v234
	v_fmac_f32_e32 v152, v139, v235
	v_fmac_f32_e32 v53, v139, v236
	v_fmac_f32_e32 v49, v139, v237
	v_fmac_f32_e32 v156, v137, v234
	v_fmac_f32_e32 v55, v137, v235
	v_fmac_f32_e32 v51, v137, v236
	v_fmac_f32_e32 v47, v137, v237
	ds_read_b128 v[234:237], v105 offset:59392
	s_waitcnt lgkmcnt(2)
	v_fmac_f32_e32 v224, v14, v242
	v_fmac_f32_e32 v223, v14, v243
	v_fmac_f32_e32 v221, v14, v244
	v_fmac_f32_e32 v217, v14, v245
	v_fmac_f32_e32 v225, v16, v242
	v_fmac_f32_e32 v222, v16, v243
	v_fmac_f32_e32 v219, v16, v244
	v_fmac_f32_e32 v215, v16, v245
	ds_read_b128 v[242:245], v105 offset:60416
	s_waitcnt lgkmcnt(2)
	v_fmac_f32_e32 v220, v14, v246
	v_fmac_f32_e32 v216, v14, v247
	v_fmac_f32_e32 v213, v14, v248
	v_fmac_f32_e32 v211, v14, v249
	v_fmac_f32_e32 v218, v16, v246
	v_fmac_f32_e32 v214, v16, v247
	v_fmac_f32_e32 v212, v16, v248
	v_fmac_f32_e32 v210, v16, v249
	ds_read_b128 v[246:249], v105 offset:61440
	s_waitcnt lgkmcnt(2)
	v_fmac_f32_e32 v209, v14, v234
	v_fmac_f32_e32 v207, v14, v235
	v_fmac_f32_e32 v205, v14, v236
	v_fmac_f32_e32 v153, v14, v237
	v_fmac_f32_e32 v208, v16, v234
	v_fmac_f32_e32 v206, v16, v235
	v_fmac_f32_e32 v158, v16, v236
	v_fmac_f32_e32 v57, v16, v237
	ds_read_b128 v[234:237], v105 offset:62464
	s_waitcnt lgkmcnt(2)
	v_fmac_f32_e32 v159, v14, v242
	v_fmac_f32_e32 v152, v14, v243
	v_fmac_f32_e32 v53, v14, v244
	v_fmac_f32_e32 v49, v14, v245
	v_fmac_f32_e32 v156, v16, v242
	v_fmac_f32_e32 v55, v16, v243
	v_fmac_f32_e32 v51, v16, v244
	v_fmac_f32_e32 v47, v16, v245
	ds_read_b128 v[242:245], v105 offset:63488
	s_waitcnt lgkmcnt(2)
	v_fmac_f32_e32 v224, v15, v246
	v_fmac_f32_e32 v223, v15, v247
	v_fmac_f32_e32 v221, v15, v248
	v_fmac_f32_e32 v217, v15, v249
	v_fmac_f32_e32 v225, v17, v246
	v_fmac_f32_e32 v222, v17, v247
	v_fmac_f32_e32 v219, v17, v248
	v_fmac_f32_e32 v215, v17, v249
	ds_read_b128 v[246:249], v105 offset:64512
	s_waitcnt lgkmcnt(2)
	v_fmac_f32_e32 v220, v15, v234
	v_fmac_f32_e32 v216, v15, v235
	v_fmac_f32_e32 v213, v15, v236
	v_fmac_f32_e32 v211, v15, v237
	v_fmac_f32_e32 v218, v17, v234
	v_fmac_f32_e32 v214, v17, v235
	v_fmac_f32_e32 v212, v17, v236
	v_fmac_f32_e32 v210, v17, v237
	s_waitcnt lgkmcnt(1)
	v_fmac_f32_e32 v57, v17, v245
	v_fmac_f32_e32 v209, v15, v242
	v_fmac_f32_e32 v207, v15, v243
	v_fmac_f32_e32 v205, v15, v244
	s_waitcnt lgkmcnt(0)
	v_fmac_f32_e32 v53, v15, v248
	v_fmac_f32_e32 v55, v17, v247
	v_fmac_f32_e32 v51, v17, v248
	v_fmac_f32_e32 v153, v15, v245
	v_fmac_f32_e32 v208, v17, v242
	v_fmac_f32_e32 v206, v17, v243
	v_fmac_f32_e32 v158, v17, v244
	v_fmac_f32_e32 v159, v15, v246
	v_fmac_f32_e32 v152, v15, v247
	v_fmac_f32_e32 v49, v15, v249
	v_fmac_f32_e32 v156, v17, v246
	v_fmac_f32_e32 v47, v17, v249
	s_waitcnt vmcnt(3)
	v_pk_add_f32 v[6:7], v[6:7], 1.0 op_sel_hi:[1,0]
	v_pk_mul_f32 v[126:127], v[102:103], v[126:127] op_sel_hi:[0,1]
	s_waitcnt vmcnt(2)
	v_pk_mul_f32 v[128:129], v[2:3], v[6:7]
	v_pk_add_f32 v[8:9], v[8:9], 1.0 op_sel_hi:[1,0]
	v_pk_fma_f32 v[130:131], v[126:127], v[128:129], v[10:11]
	v_pk_mul_f32 v[122:123], v[104:105], v[122:123] op_sel_hi:[0,1]
	v_pk_mul_f32 v[16:17], v[4:5], v[8:9]
	v_pk_mul_f32 v[14:15], v[102:103], v[124:125] op_sel_hi:[0,1]
	v_pk_mul_f32 v[120:121], v[104:105], v[120:121] op_sel_hi:[0,1]
	v_pk_fma_f32 v[128:129], v[122:123], v[128:129], v[10:11]
	v_med3_f32 v10, v130, s33, v233
	v_med3_f32 v11, v131, s33, v233
	v_mov_b32_e32 v124, 0
	v_pk_fma_f32 v[14:15], v[14:15], v[16:17], v[12:13]
	v_pk_fma_f32 v[16:17], v[120:121], v[16:17], v[12:13]
	v_cvt_pk_fp8_f32 v124, v10, v11
	v_med3_f32 v12, v128, s33, v233
	v_med3_f32 v13, v129, s33, v233
	v_mov_b32_e32 v125, 0
	v_cvt_pk_fp8_f32 v125, v12, v13
	v_med3_f32 v10, v14, s33, v233
	v_med3_f32 v11, v15, s33, v233
	v_cvt_pk_fp8_f32 v124, v10, v11 op_sel:[0,0,1]
	v_med3_f32 v10, v16, s33, v233
	v_med3_f32 v11, v17, s33, v233
	global_load_dwordx4 v[6:9], v[82:83], off
	global_load_dwordx4 v[2:5], v[84:85], off
	v_cvt_pk_fp8_f32 v125, v10, v11 op_sel:[0,0,1]
	v_add_u32_e32 v10, 0x10000, v105
	ds_read_b128 v[120:123], v10
	global_load_dwordx4 v[10:13], v[36:37], off
	s_nop 0
	global_store_dword v[118:119], v124, off offset:1024
	global_store_dword v[118:119], v125, off offset:3072
	v_add_u32_e32 v124, 0x10400, v105
	ds_read_b128 v[124:127], v124
	s_waitcnt lgkmcnt(1)
	v_fmac_f32_e32 v224, v130, v120
	v_fmac_f32_e32 v225, v128, v120
	v_add_u32_e32 v120, 0x10800, v105
	v_fmac_f32_e32 v223, v130, v121
	v_fmac_f32_e32 v221, v130, v122
	v_fmac_f32_e32 v217, v130, v123
	v_fmac_f32_e32 v222, v128, v121
	v_fmac_f32_e32 v219, v128, v122
	v_fmac_f32_e32 v215, v128, v123
	ds_read_b128 v[120:123], v120
	s_waitcnt lgkmcnt(1)
	v_fmac_f32_e32 v220, v130, v124
	v_fmac_f32_e32 v218, v128, v124
	v_add_u32_e32 v124, 0x10c00, v105
	v_fmac_f32_e32 v216, v130, v125
	v_fmac_f32_e32 v213, v130, v126
	v_fmac_f32_e32 v211, v130, v127
	v_fmac_f32_e32 v214, v128, v125
	v_fmac_f32_e32 v212, v128, v126
	v_fmac_f32_e32 v210, v128, v127
	ds_read_b128 v[124:127], v124
	s_waitcnt lgkmcnt(1)
	v_fmac_f32_e32 v209, v130, v120
	v_fmac_f32_e32 v208, v128, v120
	v_add_u32_e32 v120, 0x11000, v105
	v_fmac_f32_e32 v207, v130, v121
	v_fmac_f32_e32 v205, v130, v122
	v_fmac_f32_e32 v153, v130, v123
	v_fmac_f32_e32 v206, v128, v121
	v_fmac_f32_e32 v158, v128, v122
	v_fmac_f32_e32 v57, v128, v123
	ds_read_b128 v[120:123], v120
	s_waitcnt lgkmcnt(1)
	v_fmac_f32_e32 v159, v130, v124
	v_fmac_f32_e32 v156, v128, v124
	v_add_u32_e32 v124, 0x11400, v105
	v_fmac_f32_e32 v152, v130, v125
	v_fmac_f32_e32 v53, v130, v126
	v_fmac_f32_e32 v49, v130, v127
	v_fmac_f32_e32 v55, v128, v125
	v_fmac_f32_e32 v51, v128, v126
	v_fmac_f32_e32 v47, v128, v127
	ds_read_b128 v[124:127], v124
	s_waitcnt lgkmcnt(1)
	v_fmac_f32_e32 v224, v131, v120
	v_fmac_f32_e32 v225, v129, v120
	v_add_u32_e32 v120, 0x11800, v105
	v_fmac_f32_e32 v223, v131, v121
	v_fmac_f32_e32 v221, v131, v122
	v_fmac_f32_e32 v217, v131, v123
	v_fmac_f32_e32 v222, v129, v121
	v_fmac_f32_e32 v219, v129, v122
	v_fmac_f32_e32 v215, v129, v123
	ds_read_b128 v[120:123], v120
	s_waitcnt lgkmcnt(1)
	v_fmac_f32_e32 v220, v131, v124
	v_fmac_f32_e32 v218, v129, v124
	v_add_u32_e32 v124, 0x11c00, v105
	v_fmac_f32_e32 v216, v131, v125
	v_fmac_f32_e32 v213, v131, v126
	v_fmac_f32_e32 v211, v131, v127
	v_fmac_f32_e32 v214, v129, v125
	v_fmac_f32_e32 v212, v129, v126
	v_fmac_f32_e32 v210, v129, v127
	ds_read_b128 v[124:127], v124
	s_waitcnt lgkmcnt(1)
	v_fmac_f32_e32 v209, v131, v120
	v_fmac_f32_e32 v208, v129, v120
	v_add_u32_e32 v120, 0x12000, v105
	v_fmac_f32_e32 v207, v131, v121
	v_fmac_f32_e32 v205, v131, v122
	v_fmac_f32_e32 v153, v131, v123
	v_fmac_f32_e32 v206, v129, v121
	v_fmac_f32_e32 v158, v129, v122
	v_fmac_f32_e32 v57, v129, v123
	ds_read_b128 v[120:123], v120
	s_waitcnt lgkmcnt(1)
	v_fmac_f32_e32 v159, v131, v124
	v_fmac_f32_e32 v156, v129, v124
	v_add_u32_e32 v124, 0x12400, v105
	v_fmac_f32_e32 v152, v131, v125
	v_fmac_f32_e32 v53, v131, v126
	v_fmac_f32_e32 v49, v131, v127
	v_fmac_f32_e32 v55, v129, v125
	v_fmac_f32_e32 v51, v129, v126
	v_fmac_f32_e32 v47, v129, v127
	ds_read_b128 v[124:127], v124
	s_waitcnt lgkmcnt(1)
	v_fmac_f32_e32 v224, v14, v120
	v_fmac_f32_e32 v225, v16, v120
	v_add_u32_e32 v120, 0x12800, v105
	v_fmac_f32_e32 v223, v14, v121
	v_fmac_f32_e32 v221, v14, v122
	v_fmac_f32_e32 v217, v14, v123
	v_fmac_f32_e32 v222, v16, v121
	v_fmac_f32_e32 v219, v16, v122
	v_fmac_f32_e32 v215, v16, v123
	ds_read_b128 v[120:123], v120
	s_waitcnt lgkmcnt(1)
	v_fmac_f32_e32 v220, v14, v124
	v_fmac_f32_e32 v218, v16, v124
	v_add_u32_e32 v124, 0x12c00, v105
	v_fmac_f32_e32 v216, v14, v125
	v_fmac_f32_e32 v213, v14, v126
	v_fmac_f32_e32 v211, v14, v127
	v_fmac_f32_e32 v214, v16, v125
	v_fmac_f32_e32 v212, v16, v126
	v_fmac_f32_e32 v210, v16, v127
	ds_read_b128 v[124:127], v124
	s_waitcnt lgkmcnt(1)
	v_fmac_f32_e32 v209, v14, v120
	v_fmac_f32_e32 v207, v14, v121
	v_fmac_f32_e32 v205, v14, v122
	v_fmac_f32_e32 v153, v14, v123
	s_waitcnt lgkmcnt(0)
	v_fmac_f32_e32 v159, v14, v124
	v_fmac_f32_e32 v152, v14, v125
	v_fmac_f32_e32 v53, v14, v126
	v_fmac_f32_e32 v49, v14, v127
	v_add_u32_e32 v14, 0x13000, v105
	v_fmac_f32_e32 v208, v16, v120
	v_fmac_f32_e32 v206, v16, v121
	v_fmac_f32_e32 v158, v16, v122
	v_fmac_f32_e32 v57, v16, v123
	ds_read_b128 v[120:123], v14
	v_add_u32_e32 v14, 0x13400, v105
	v_fmac_f32_e32 v156, v16, v124
	v_fmac_f32_e32 v55, v16, v125
	v_fmac_f32_e32 v51, v16, v126
	v_fmac_f32_e32 v47, v16, v127
	ds_read_b128 v[124:127], v14
	v_add_u32_e32 v14, 0x13800, v105
	s_waitcnt lgkmcnt(1)
	v_fmac_f32_e32 v224, v15, v120
	v_fmac_f32_e32 v223, v15, v121
	v_fmac_f32_e32 v221, v15, v122
	v_fmac_f32_e32 v217, v15, v123
	v_fmac_f32_e32 v225, v17, v120
	v_fmac_f32_e32 v222, v17, v121
	v_fmac_f32_e32 v219, v17, v122
	v_fmac_f32_e32 v215, v17, v123
	ds_read_b128 v[120:123], v14
	v_add_u32_e32 v14, 0x13c00, v105
	s_waitcnt lgkmcnt(1)
	v_fmac_f32_e32 v220, v15, v124
	v_fmac_f32_e32 v216, v15, v125
	v_fmac_f32_e32 v213, v15, v126
	v_fmac_f32_e32 v211, v15, v127
	v_fmac_f32_e32 v218, v17, v124
	v_fmac_f32_e32 v214, v17, v125
	v_fmac_f32_e32 v212, v17, v126
	v_fmac_f32_e32 v210, v17, v127
	ds_read_b128 v[124:127], v14
	s_waitcnt lgkmcnt(1)
	v_fmac_f32_e32 v57, v17, v123
	v_fmac_f32_e32 v209, v15, v120
	v_fmac_f32_e32 v207, v15, v121
	v_fmac_f32_e32 v205, v15, v122
	s_waitcnt lgkmcnt(0)
	v_fmac_f32_e32 v53, v15, v126
	v_fmac_f32_e32 v55, v17, v125
	v_fmac_f32_e32 v51, v17, v126
	v_fmac_f32_e32 v153, v15, v123
	v_fmac_f32_e32 v208, v17, v120
	v_fmac_f32_e32 v206, v17, v121
	v_fmac_f32_e32 v158, v17, v122
	v_fmac_f32_e32 v159, v15, v124
	v_fmac_f32_e32 v152, v15, v125
	v_fmac_f32_e32 v49, v15, v127
	v_fmac_f32_e32 v156, v17, v124
	v_fmac_f32_e32 v47, v17, v127
	s_waitcnt vmcnt(3)
	v_pk_add_f32 v[2:3], v[2:3], 1.0 op_sel_hi:[1,0]
	v_pk_mul_f32 v[116:117], v[102:103], v[116:117] op_sel_hi:[0,1]
	s_waitcnt vmcnt(2)
	v_pk_mul_f32 v[120:121], v[10:11], v[2:3]
	v_pk_add_f32 v[4:5], v[4:5], 1.0 op_sel_hi:[1,0]
	v_pk_fma_f32 v[122:123], v[116:117], v[120:121], v[6:7]
	v_pk_mul_f32 v[112:113], v[104:105], v[112:113] op_sel_hi:[0,1]
	v_pk_mul_f32 v[16:17], v[12:13], v[4:5]
	v_pk_mul_f32 v[14:15], v[102:103], v[114:115] op_sel_hi:[0,1]
	v_pk_mul_f32 v[110:111], v[104:105], v[110:111] op_sel_hi:[0,1]
	v_pk_fma_f32 v[120:121], v[112:113], v[120:121], v[6:7]
	v_med3_f32 v6, v122, s33, v233
	v_med3_f32 v7, v123, s33, v233
	v_mov_b32_e32 v114, 0
	v_pk_fma_f32 v[14:15], v[14:15], v[16:17], v[8:9]
	v_pk_fma_f32 v[16:17], v[110:111], v[16:17], v[8:9]
	v_cvt_pk_fp8_f32 v114, v6, v7
	v_med3_f32 v8, v120, s33, v233
	v_med3_f32 v9, v121, s33, v233
	v_mov_b32_e32 v115, 0
	v_cvt_pk_fp8_f32 v115, v8, v9
	v_med3_f32 v6, v14, s33, v233
	v_med3_f32 v7, v15, s33, v233
	v_cvt_pk_fp8_f32 v114, v6, v7 op_sel:[0,0,1]
	v_med3_f32 v6, v16, s33, v233
	v_med3_f32 v7, v17, s33, v233
	v_cvt_pk_fp8_f32 v115, v6, v7 op_sel:[0,0,1]
	v_add_u32_e32 v6, 0x14000, v105
	global_load_dwordx4 v[2:5], v[86:87], off
	global_load_dwordx4 v[10:13], v[88:89], off
	ds_read_b128 v[110:113], v6
	global_load_dwordx4 v[6:9], v[38:39], off
	s_nop 0
	global_store_dword v[118:119], v114, off offset:1280
	global_store_dword v[118:119], v115, off offset:3328
	v_add_u32_e32 v114, 0x14400, v105
	ds_read_b128 v[114:117], v114
	s_waitcnt lgkmcnt(1)
	v_fmac_f32_e32 v224, v122, v110
	v_fmac_f32_e32 v225, v120, v110
	v_add_u32_e32 v110, 0x14800, v105
	v_fmac_f32_e32 v223, v122, v111
	v_fmac_f32_e32 v221, v122, v112
	v_fmac_f32_e32 v217, v122, v113
	v_fmac_f32_e32 v222, v120, v111
	v_fmac_f32_e32 v219, v120, v112
	v_fmac_f32_e32 v215, v120, v113
	ds_read_b128 v[110:113], v110
	s_waitcnt lgkmcnt(1)
	v_fmac_f32_e32 v220, v122, v114
	v_fmac_f32_e32 v218, v120, v114
	v_add_u32_e32 v114, 0x14c00, v105
	v_fmac_f32_e32 v216, v122, v115
	v_fmac_f32_e32 v213, v122, v116
	v_fmac_f32_e32 v211, v122, v117
	v_fmac_f32_e32 v214, v120, v115
	v_fmac_f32_e32 v212, v120, v116
	v_fmac_f32_e32 v210, v120, v117
	ds_read_b128 v[114:117], v114
	s_waitcnt lgkmcnt(1)
	v_fmac_f32_e32 v209, v122, v110
	v_fmac_f32_e32 v208, v120, v110
	v_add_u32_e32 v110, 0x15000, v105
	v_fmac_f32_e32 v207, v122, v111
	v_fmac_f32_e32 v205, v122, v112
	v_fmac_f32_e32 v153, v122, v113
	v_fmac_f32_e32 v206, v120, v111
	v_fmac_f32_e32 v158, v120, v112
	v_fmac_f32_e32 v57, v120, v113
	ds_read_b128 v[110:113], v110
	s_waitcnt lgkmcnt(1)
	v_fmac_f32_e32 v159, v122, v114
	v_fmac_f32_e32 v152, v122, v115
	v_fmac_f32_e32 v53, v122, v116
	v_fmac_f32_e32 v49, v122, v117
	v_fmac_f32_e32 v156, v120, v114
	v_fmac_f32_e32 v55, v120, v115
	v_fmac_f32_e32 v51, v120, v116
	v_fmac_f32_e32 v47, v120, v117
	ds_read_b128 v[114:117], v230
	s_waitcnt lgkmcnt(1)
	v_fmac_f32_e32 v224, v123, v110
	v_fmac_f32_e32 v223, v123, v111
	v_fmac_f32_e32 v221, v123, v112
	v_fmac_f32_e32 v217, v123, v113
	v_fmac_f32_e32 v225, v121, v110
	v_fmac_f32_e32 v222, v121, v111
	v_fmac_f32_e32 v219, v121, v112
	v_fmac_f32_e32 v215, v121, v113
	ds_read_b128 v[110:113], v250
	s_waitcnt lgkmcnt(1)
	v_fmac_f32_e32 v220, v123, v114
	v_fmac_f32_e32 v216, v123, v115
	v_fmac_f32_e32 v213, v123, v116
	v_fmac_f32_e32 v211, v123, v117
	v_fmac_f32_e32 v218, v121, v114
	v_fmac_f32_e32 v214, v121, v115
	v_fmac_f32_e32 v212, v121, v116
	v_fmac_f32_e32 v210, v121, v117
	ds_read_b128 v[114:117], v251
	s_waitcnt lgkmcnt(1)
	v_fmac_f32_e32 v209, v123, v110
	v_fmac_f32_e32 v207, v123, v111
	v_fmac_f32_e32 v205, v123, v112
	v_fmac_f32_e32 v153, v123, v113
	v_fmac_f32_e32 v208, v121, v110
	v_fmac_f32_e32 v206, v121, v111
	v_fmac_f32_e32 v158, v121, v112
	v_fmac_f32_e32 v57, v121, v113
	s_waitcnt lgkmcnt(0)
	v_fmac_f32_e32 v159, v123, v114
	v_fmac_f32_e32 v152, v123, v115
	v_fmac_f32_e32 v53, v123, v116
	v_fmac_f32_e32 v49, v123, v117
	v_fmac_f32_e32 v156, v121, v114
	ds_read_b128 v[110:113], v164
	v_fmac_f32_e32 v55, v121, v115
	v_fmac_f32_e32 v51, v121, v116
	v_fmac_f32_e32 v47, v121, v117
	ds_read_b128 v[114:117], v165
	s_waitcnt lgkmcnt(1)
	v_fmac_f32_e32 v224, v14, v110
	v_fmac_f32_e32 v223, v14, v111
	v_fmac_f32_e32 v221, v14, v112
	v_fmac_f32_e32 v217, v14, v113
	v_fmac_f32_e32 v225, v16, v110
	v_fmac_f32_e32 v222, v16, v111
	v_fmac_f32_e32 v219, v16, v112
	v_fmac_f32_e32 v215, v16, v113
	s_waitcnt lgkmcnt(0)
	v_fmac_f32_e32 v220, v14, v114
	v_fmac_f32_e32 v216, v14, v115
	v_fmac_f32_e32 v213, v14, v116
	v_fmac_f32_e32 v211, v14, v117
	v_fmac_f32_e32 v218, v16, v114
	ds_read_b128 v[110:113], v166
	v_fmac_f32_e32 v214, v16, v115
	v_fmac_f32_e32 v212, v16, v116
	v_fmac_f32_e32 v210, v16, v117
	ds_read_b128 v[114:117], v167
	s_waitcnt lgkmcnt(1)
	v_fmac_f32_e32 v209, v14, v110
	v_fmac_f32_e32 v207, v14, v111
	v_fmac_f32_e32 v205, v14, v112
	v_fmac_f32_e32 v153, v14, v113
	v_fmac_f32_e32 v208, v16, v110
	v_fmac_f32_e32 v206, v16, v111
	v_fmac_f32_e32 v158, v16, v112
	v_fmac_f32_e32 v57, v16, v113
	s_waitcnt lgkmcnt(0)
	v_fmac_f32_e32 v159, v14, v114
	v_fmac_f32_e32 v152, v14, v115
	v_fmac_f32_e32 v53, v14, v116
	v_fmac_f32_e32 v49, v14, v117
	v_fmac_f32_e32 v156, v16, v114
	ds_read_b128 v[110:113], v168
	v_fmac_f32_e32 v55, v16, v115
	v_fmac_f32_e32 v51, v16, v116
	v_fmac_f32_e32 v47, v16, v117
	ds_read_b128 v[114:117], v169
	s_waitcnt lgkmcnt(1)
	v_fmac_f32_e32 v224, v15, v110
	v_fmac_f32_e32 v223, v15, v111
	v_fmac_f32_e32 v221, v15, v112
	v_fmac_f32_e32 v217, v15, v113
	v_fmac_f32_e32 v225, v17, v110
	v_fmac_f32_e32 v222, v17, v111
	v_fmac_f32_e32 v219, v17, v112
	v_fmac_f32_e32 v215, v17, v113
	s_waitcnt lgkmcnt(0)
	v_fmac_f32_e32 v220, v15, v114
	v_fmac_f32_e32 v216, v15, v115
	v_fmac_f32_e32 v213, v15, v116
	v_fmac_f32_e32 v211, v15, v117
	v_fmac_f32_e32 v218, v17, v114
	ds_read_b128 v[110:113], v170
	v_fmac_f32_e32 v214, v17, v115
	v_fmac_f32_e32 v212, v17, v116
	v_fmac_f32_e32 v210, v17, v117
	ds_read_b128 v[114:117], v171
	s_waitcnt lgkmcnt(1)
	v_fmac_f32_e32 v57, v17, v113
	v_fmac_f32_e32 v209, v15, v110
	v_fmac_f32_e32 v207, v15, v111
	v_fmac_f32_e32 v205, v15, v112
	s_waitcnt lgkmcnt(0)
	v_fmac_f32_e32 v53, v15, v116
	v_fmac_f32_e32 v55, v17, v115
	v_fmac_f32_e32 v51, v17, v116
	v_fmac_f32_e32 v153, v15, v113
	v_fmac_f32_e32 v208, v17, v110
	v_fmac_f32_e32 v206, v17, v111
	v_fmac_f32_e32 v158, v17, v112
	v_fmac_f32_e32 v159, v15, v114
	v_fmac_f32_e32 v152, v15, v115
	v_fmac_f32_e32 v49, v15, v117
	v_fmac_f32_e32 v156, v17, v114
	v_fmac_f32_e32 v47, v17, v117
	s_waitcnt vmcnt(3)
	v_pk_add_f32 v[12:13], v[12:13], 1.0 op_sel_hi:[1,0]
	v_pk_add_f32 v[10:11], v[10:11], 1.0 op_sel_hi:[1,0]
	s_waitcnt vmcnt(2)
	v_pk_mul_f32 v[12:13], v[8:9], v[12:13]
	v_pk_mul_f32 v[10:11], v[6:7], v[10:11]
	global_load_dwordx4 v[6:9], v[90:91], off
	global_load_dwordx4 v[114:117], v[92:93], off
	global_load_dwordx4 v[120:123], v[40:41], off
	v_pk_mul_f32 v[14:15], v[102:103], v[108:109] op_sel_hi:[0,1]
	v_pk_mul_f32 v[16:17], v[102:103], v[106:107] op_sel_hi:[0,1]
	v_pk_fma_f32 v[106:107], v[16:17], v[12:13], v[4:5]
	v_pk_fma_f32 v[108:109], v[14:15], v[10:11], v[2:3]
	v_pk_mul_f32 v[14:15], v[104:105], v[20:21] op_sel_hi:[0,1]
	v_pk_mul_f32 v[16:17], v[104:105], v[18:19] op_sel_hi:[0,1]
	v_pk_fma_f32 v[110:111], v[16:17], v[12:13], v[4:5]
	v_pk_fma_f32 v[112:113], v[14:15], v[10:11], v[2:3]
	v_med3_f32 v2, v108, s33, v233
	v_med3_f32 v3, v109, s33, v233
	v_mov_b32_e32 v4, 0
	v_cvt_pk_fp8_f32 v4, v2, v3
	v_med3_f32 v2, v106, s33, v233
	v_med3_f32 v3, v107, s33, v233
	v_cvt_pk_fp8_f32 v4, v2, v3 op_sel:[0,0,1]
	v_med3_f32 v2, v112, s33, v233
	v_med3_f32 v3, v113, s33, v233
	global_store_dword v[118:119], v4, off offset:1536
	v_mov_b32_e32 v4, 0
	v_cvt_pk_fp8_f32 v4, v2, v3
	v_med3_f32 v2, v110, s33, v233
	v_med3_f32 v3, v111, s33, v233
	v_cvt_pk_fp8_f32 v4, v2, v3 op_sel:[0,0,1]
	global_store_dword v[118:119], v4, off offset:3584
	ds_read_b128 v[10:13], v172
	ds_read_b128 v[124:127], v173
	ds_read_b128 v[128:131], v174
	ds_read_b128 v[132:135], v175
	ds_read_b128 v[14:17], v176
	ds_read_b128 v[136:139], v177
	ds_read_b128 v[140:143], v178
	ds_read_b128 v[144:147], v179
	ds_read_b128 v[18:21], v180
	ds_read_b128 v[148:151], v181
	ds_read_b128 v[238:241], v182
	ds_read_b128 v[242:245], v183
	ds_read_b128 v[2:5], v184
	ds_read_b128 v[246:249], v185
	ds_read_b128 v[234:237], v186
	ds_read_b128 v[160:163], v187
	s_waitcnt vmcnt(3)
	v_pk_add_f32 v[116:117], v[116:117], 1.0 op_sel_hi:[1,0]
	v_pk_add_f32 v[154:155], v[114:115], 1.0 op_sel_hi:[1,0]
	s_waitcnt lgkmcnt(14)
	v_fmac_f32_e32 v215, v112, v13
	v_fmac_f32_e32 v219, v112, v12
	v_fmac_f32_e32 v222, v112, v11
	v_fmac_f32_e32 v225, v112, v10
	v_fmac_f32_e32 v217, v108, v13
	v_fmac_f32_e32 v221, v108, v12
	v_fmac_f32_e32 v223, v108, v11
	v_fmac_f32_e32 v224, v108, v10
	s_waitcnt vmcnt(2)
	v_pk_mul_f32 v[114:115], v[122:123], v[116:117]
	v_pk_mul_f32 v[116:117], v[120:121], v[154:155]
	s_waitcnt lgkmcnt(11)
	v_fmac_f32_e32 v215, v113, v17
	v_fmac_f32_e32 v219, v113, v16
	v_fmac_f32_e32 v222, v113, v15
	v_fmac_f32_e32 v225, v113, v14
	v_fmac_f32_e32 v217, v109, v17
	v_fmac_f32_e32 v221, v109, v16
	v_fmac_f32_e32 v223, v109, v15
	v_fmac_f32_e32 v224, v109, v14
	v_pk_mul_f32 v[10:11], v[102:103], v[100:101] op_sel_hi:[0,1]
	s_waitcnt lgkmcnt(7)
	v_fmac_f32_e32 v215, v110, v21
	v_fmac_f32_e32 v219, v110, v20
	v_fmac_f32_e32 v222, v110, v19
	v_fmac_f32_e32 v225, v110, v18
	v_fmac_f32_e32 v217, v106, v21
	v_fmac_f32_e32 v221, v106, v20
	v_fmac_f32_e32 v223, v106, v19
	v_fmac_f32_e32 v224, v106, v18
	v_pk_fma_f32 v[18:19], v[10:11], v[116:117], v[6:7]
	v_pk_mul_f32 v[10:11], v[104:105], v[96:97] op_sel_hi:[0,1]
	s_waitcnt lgkmcnt(3)
	v_fmac_f32_e32 v215, v111, v5
	v_fmac_f32_e32 v219, v111, v4
	v_fmac_f32_e32 v222, v111, v3
	v_fmac_f32_e32 v217, v107, v5
	v_fmac_f32_e32 v221, v107, v4
	v_fmac_f32_e32 v223, v107, v3
	v_pk_mul_f32 v[4:5], v[102:103], v[98:99] op_sel_hi:[0,1]
	v_pk_mul_f32 v[12:13], v[104:105], v[94:95] op_sel_hi:[0,1]
	v_pk_fma_f32 v[6:7], v[10:11], v[116:117], v[6:7]
	v_med3_f32 v3, v18, s33, v233
	v_med3_f32 v10, v19, s33, v233
	v_mov_b32_e32 v14, 0
	v_pk_fma_f32 v[4:5], v[4:5], v[114:115], v[8:9]
	v_pk_fma_f32 v[8:9], v[12:13], v[114:115], v[8:9]
	v_cvt_pk_fp8_f32 v14, v3, v10
	v_med3_f32 v11, v6, s33, v233
	v_med3_f32 v12, v7, s33, v233
	v_mov_b32_e32 v15, 0
	v_cvt_pk_fp8_f32 v15, v11, v12
	v_med3_f32 v3, v4, s33, v233
	v_med3_f32 v10, v5, s33, v233
	v_cvt_pk_fp8_f32 v14, v3, v10 op_sel:[0,0,1]
	v_med3_f32 v3, v8, s33, v233
	v_med3_f32 v10, v9, s33, v233
	v_cvt_pk_fp8_f32 v15, v3, v10 op_sel:[0,0,1]
	ds_read_b128 v[10:13], v188
	global_store_dword v[118:119], v14, off offset:1792
	global_store_dword v[118:119], v15, off offset:3840
	ds_read_b128 v[14:17], v189
	v_fmac_f32_e32 v210, v112, v127
	v_fmac_f32_e32 v212, v112, v126
	v_fmac_f32_e32 v214, v112, v125
	v_fmac_f32_e32 v218, v112, v124
	v_fmac_f32_e32 v211, v108, v127
	v_fmac_f32_e32 v213, v108, v126
	v_fmac_f32_e32 v216, v108, v125
	v_fmac_f32_e32 v220, v108, v124
	v_fmac_f32_e32 v210, v113, v139
	v_fmac_f32_e32 v212, v113, v138
	v_fmac_f32_e32 v214, v113, v137
	v_fmac_f32_e32 v218, v113, v136
	v_fmac_f32_e32 v211, v109, v139
	v_fmac_f32_e32 v213, v109, v138
	v_fmac_f32_e32 v216, v109, v137
	v_fmac_f32_e32 v220, v109, v136
	v_fmac_f32_e32 v210, v110, v151
	v_fmac_f32_e32 v212, v110, v150
	v_fmac_f32_e32 v214, v110, v149
	v_fmac_f32_e32 v218, v110, v148
	v_fmac_f32_e32 v211, v106, v151
	v_fmac_f32_e32 v213, v106, v150
	v_fmac_f32_e32 v216, v106, v149
	v_fmac_f32_e32 v220, v106, v148
	s_waitcnt lgkmcnt(4)
	v_fmac_f32_e32 v210, v111, v249
	v_fmac_f32_e32 v212, v111, v248
	v_fmac_f32_e32 v214, v111, v247
	v_fmac_f32_e32 v218, v111, v246
	v_fmac_f32_e32 v211, v107, v249
	v_fmac_f32_e32 v213, v107, v248
	v_fmac_f32_e32 v216, v107, v247
	v_fmac_f32_e32 v220, v107, v246
	v_fmac_f32_e32 v225, v111, v2
	v_fmac_f32_e32 v224, v107, v2
	s_waitcnt lgkmcnt(1)
	v_fmac_f32_e32 v224, v18, v10
	v_fmac_f32_e32 v223, v18, v11
	v_fmac_f32_e32 v221, v18, v12
	v_fmac_f32_e32 v217, v18, v13
	v_fmac_f32_e32 v225, v6, v10
	v_fmac_f32_e32 v222, v6, v11
	v_fmac_f32_e32 v219, v6, v12
	v_fmac_f32_e32 v215, v6, v13
	ds_read_b128 v[10:13], v190
	s_waitcnt lgkmcnt(1)
	v_fmac_f32_e32 v220, v18, v14
	v_fmac_f32_e32 v216, v18, v15
	v_fmac_f32_e32 v213, v18, v16
	v_fmac_f32_e32 v211, v18, v17
	v_fmac_f32_e32 v218, v6, v14
	v_fmac_f32_e32 v214, v6, v15
	v_fmac_f32_e32 v212, v6, v16
	v_fmac_f32_e32 v210, v6, v17
	ds_read_b128 v[14:17], v191
	v_fmac_f32_e32 v47, v112, v135
	v_fmac_f32_e32 v51, v112, v134
	v_fmac_f32_e32 v55, v112, v133
	v_fmac_f32_e32 v156, v112, v132
	v_fmac_f32_e32 v49, v108, v135
	v_fmac_f32_e32 v53, v108, v134
	v_fmac_f32_e32 v152, v108, v133
	v_fmac_f32_e32 v159, v108, v132
	v_fmac_f32_e32 v57, v112, v131
	v_fmac_f32_e32 v158, v112, v130
	v_fmac_f32_e32 v206, v112, v129
	v_fmac_f32_e32 v208, v112, v128
	v_fmac_f32_e32 v153, v108, v131
	v_fmac_f32_e32 v205, v108, v130
	v_fmac_f32_e32 v207, v108, v129
	v_fmac_f32_e32 v209, v108, v128
	v_fmac_f32_e32 v47, v113, v147
	v_fmac_f32_e32 v51, v113, v146
	v_fmac_f32_e32 v55, v113, v145
	v_fmac_f32_e32 v156, v113, v144
	v_fmac_f32_e32 v49, v109, v147
	v_fmac_f32_e32 v53, v109, v146
	v_fmac_f32_e32 v152, v109, v145
	v_fmac_f32_e32 v159, v109, v144
	v_fmac_f32_e32 v57, v113, v143
	v_fmac_f32_e32 v158, v113, v142
	v_fmac_f32_e32 v206, v113, v141
	v_fmac_f32_e32 v208, v113, v140
	v_fmac_f32_e32 v153, v109, v143
	v_fmac_f32_e32 v205, v109, v142
	v_fmac_f32_e32 v207, v109, v141
	v_fmac_f32_e32 v209, v109, v140
	v_fmac_f32_e32 v47, v110, v245
	v_fmac_f32_e32 v51, v110, v244
	v_fmac_f32_e32 v55, v110, v243
	v_fmac_f32_e32 v156, v110, v242
	v_fmac_f32_e32 v49, v106, v245
	v_fmac_f32_e32 v53, v106, v244
	v_fmac_f32_e32 v152, v106, v243
	v_fmac_f32_e32 v159, v106, v242
	v_fmac_f32_e32 v57, v110, v241
	v_fmac_f32_e32 v158, v110, v240
	v_fmac_f32_e32 v206, v110, v239
	v_fmac_f32_e32 v208, v110, v238
	v_fmac_f32_e32 v153, v106, v241
	v_fmac_f32_e32 v205, v106, v240
	v_fmac_f32_e32 v207, v106, v239
	v_fmac_f32_e32 v209, v106, v238
	v_fmac_f32_e32 v47, v111, v163
	v_fmac_f32_e32 v51, v111, v162
	v_fmac_f32_e32 v55, v111, v161
	v_fmac_f32_e32 v156, v111, v160
	v_fmac_f32_e32 v49, v107, v163
	v_fmac_f32_e32 v53, v107, v162
	v_fmac_f32_e32 v152, v107, v161
	v_fmac_f32_e32 v159, v107, v160
	v_fmac_f32_e32 v57, v111, v237
	v_fmac_f32_e32 v158, v111, v236
	v_fmac_f32_e32 v206, v111, v235
	v_fmac_f32_e32 v208, v111, v234
	v_fmac_f32_e32 v153, v107, v237
	v_fmac_f32_e32 v205, v107, v236
	v_fmac_f32_e32 v207, v107, v235
	v_fmac_f32_e32 v209, v107, v234
	s_waitcnt lgkmcnt(1)
	v_fmac_f32_e32 v209, v18, v10
	v_fmac_f32_e32 v207, v18, v11
	v_fmac_f32_e32 v205, v18, v12
	v_fmac_f32_e32 v153, v18, v13
	v_fmac_f32_e32 v208, v6, v10
	v_fmac_f32_e32 v206, v6, v11
	v_fmac_f32_e32 v158, v6, v12
	v_fmac_f32_e32 v57, v6, v13
	ds_read_b128 v[10:13], v192
	s_waitcnt lgkmcnt(1)
	v_fmac_f32_e32 v159, v18, v14
	v_fmac_f32_e32 v152, v18, v15
	v_fmac_f32_e32 v53, v18, v16
	v_fmac_f32_e32 v49, v18, v17
	v_fmac_f32_e32 v156, v6, v14
	v_fmac_f32_e32 v55, v6, v15
	v_fmac_f32_e32 v51, v6, v16
	v_fmac_f32_e32 v47, v6, v17
	ds_read_b128 v[14:17], v193
	s_waitcnt lgkmcnt(1)
	v_fmac_f32_e32 v224, v19, v10
	v_fmac_f32_e32 v223, v19, v11
	v_fmac_f32_e32 v221, v19, v12
	v_fmac_f32_e32 v217, v19, v13
	v_fmac_f32_e32 v225, v7, v10
	v_fmac_f32_e32 v222, v7, v11
	v_fmac_f32_e32 v219, v7, v12
	v_fmac_f32_e32 v215, v7, v13
	ds_read_b128 v[10:13], v194
	s_waitcnt lgkmcnt(1)
	v_fmac_f32_e32 v220, v19, v14
	v_fmac_f32_e32 v216, v19, v15
	v_fmac_f32_e32 v213, v19, v16
	v_fmac_f32_e32 v211, v19, v17
	v_fmac_f32_e32 v218, v7, v14
	v_fmac_f32_e32 v214, v7, v15
	v_fmac_f32_e32 v212, v7, v16
	v_fmac_f32_e32 v210, v7, v17
	ds_read_b128 v[14:17], v195
	s_waitcnt lgkmcnt(1)
	v_fmac_f32_e32 v209, v19, v10
	v_fmac_f32_e32 v207, v19, v11
	v_fmac_f32_e32 v205, v19, v12
	v_fmac_f32_e32 v153, v19, v13
	v_fmac_f32_e32 v208, v7, v10
	v_fmac_f32_e32 v206, v7, v11
	v_fmac_f32_e32 v158, v7, v12
	v_fmac_f32_e32 v57, v7, v13
	ds_read_b128 v[10:13], v196
	s_waitcnt lgkmcnt(1)
	v_fmac_f32_e32 v159, v19, v14
	v_fmac_f32_e32 v152, v19, v15
	v_fmac_f32_e32 v53, v19, v16
	v_fmac_f32_e32 v49, v19, v17
	v_fmac_f32_e32 v156, v7, v14
	v_fmac_f32_e32 v55, v7, v15
	v_fmac_f32_e32 v51, v7, v16
	v_fmac_f32_e32 v47, v7, v17
	ds_read_b128 v[14:17], v197
	s_waitcnt lgkmcnt(1)
	v_fmac_f32_e32 v224, v4, v10
	v_fmac_f32_e32 v223, v4, v11
	v_fmac_f32_e32 v221, v4, v12
	v_fmac_f32_e32 v217, v4, v13
	v_fmac_f32_e32 v225, v8, v10
	v_fmac_f32_e32 v222, v8, v11
	v_fmac_f32_e32 v219, v8, v12
	v_fmac_f32_e32 v215, v8, v13
	ds_read_b128 v[10:13], v198
	s_waitcnt lgkmcnt(1)
	v_fmac_f32_e32 v220, v4, v14
	v_fmac_f32_e32 v216, v4, v15
	v_fmac_f32_e32 v213, v4, v16
	v_fmac_f32_e32 v211, v4, v17
	v_fmac_f32_e32 v218, v8, v14
	v_fmac_f32_e32 v214, v8, v15
	v_fmac_f32_e32 v212, v8, v16
	v_fmac_f32_e32 v210, v8, v17
	ds_read_b128 v[14:17], v199
	s_waitcnt lgkmcnt(1)
	v_fmac_f32_e32 v209, v4, v10
	v_fmac_f32_e32 v207, v4, v11
	v_fmac_f32_e32 v205, v4, v12
	v_fmac_f32_e32 v153, v4, v13
	v_fmac_f32_e32 v208, v8, v10
	v_fmac_f32_e32 v206, v8, v11
	v_fmac_f32_e32 v158, v8, v12
	v_fmac_f32_e32 v57, v8, v13
	ds_read_b128 v[10:13], v200
	s_waitcnt lgkmcnt(1)
	v_fmac_f32_e32 v159, v4, v14
	v_fmac_f32_e32 v152, v4, v15
	v_fmac_f32_e32 v53, v4, v16
	v_fmac_f32_e32 v49, v4, v17
	v_fmac_f32_e32 v156, v8, v14
	v_fmac_f32_e32 v55, v8, v15
	v_fmac_f32_e32 v51, v8, v16
	v_fmac_f32_e32 v47, v8, v17
	ds_read_b128 v[14:17], v201
	s_waitcnt lgkmcnt(1)
	v_fmac_f32_e32 v224, v5, v10
	v_fmac_f32_e32 v223, v5, v11
	v_fmac_f32_e32 v221, v5, v12
	v_fmac_f32_e32 v217, v5, v13
	v_fmac_f32_e32 v225, v9, v10
	v_fmac_f32_e32 v222, v9, v11
	v_fmac_f32_e32 v219, v9, v12
	v_fmac_f32_e32 v215, v9, v13
	ds_read_b128 v[10:13], v202
	s_waitcnt lgkmcnt(1)
	v_fmac_f32_e32 v220, v5, v14
	v_fmac_f32_e32 v216, v5, v15
	v_fmac_f32_e32 v213, v5, v16
	v_fmac_f32_e32 v211, v5, v17
	v_fmac_f32_e32 v218, v9, v14
	v_fmac_f32_e32 v214, v9, v15
	v_fmac_f32_e32 v212, v9, v16
	v_fmac_f32_e32 v210, v9, v17
	ds_read_b128 v[14:17], v203
	s_waitcnt lgkmcnt(1)
	v_fmac_f32_e32 v57, v9, v13
	v_fmac_f32_e32 v209, v5, v10
	v_fmac_f32_e32 v207, v5, v11
	v_fmac_f32_e32 v205, v5, v12
	s_waitcnt lgkmcnt(0)
	v_fmac_f32_e32 v53, v5, v16
	v_fmac_f32_e32 v55, v9, v15
	v_fmac_f32_e32 v51, v9, v16
	v_fmac_f32_e32 v153, v5, v13
	v_fmac_f32_e32 v208, v9, v10
	v_fmac_f32_e32 v206, v9, v11
	v_fmac_f32_e32 v158, v9, v12
	v_fmac_f32_e32 v159, v5, v14
	v_fmac_f32_e32 v152, v5, v15
	v_fmac_f32_e32 v49, v5, v17
	v_fmac_f32_e32 v156, v9, v14
	v_fmac_f32_e32 v47, v9, v17
	v_mov_b32_dpp v10, v221 quad_perm:[1,0,3,2] row_mask:0xf bank_mask:0xf
	v_mov_b32_dpp v12, v219 quad_perm:[1,0,3,2] row_mask:0xf bank_mask:0xf
	v_mov_b32_dpp v14, v217 quad_perm:[1,0,3,2] row_mask:0xf bank_mask:0xf
	v_mov_b32_dpp v2, v224 quad_perm:[1,0,3,2] row_mask:0xf bank_mask:0xf
	v_mov_b32_dpp v3, v225 quad_perm:[1,0,3,2] row_mask:0xf bank_mask:0xf
	s_waitcnt lgkmcnt(4)
	v_add_f32_e32 v10, v221, v10
	s_nop 1
	v_mov_b32_dpp v11, v10 quad_perm:[2,3,0,1] row_mask:0xf bank_mask:0xf
	s_waitcnt lgkmcnt(4)
	v_add_f32_e32 v12, v219, v12
	s_nop 1
	v_mov_b32_dpp v13, v12 quad_perm:[2,3,0,1] row_mask:0xf bank_mask:0xf
	v_mov_b32_dpp v6, v223 quad_perm:[1,0,3,2] row_mask:0xf bank_mask:0xf
	v_mov_b32_dpp v8, v222 quad_perm:[1,0,3,2] row_mask:0xf bank_mask:0xf
	s_waitcnt lgkmcnt(3)
	v_add_f32_e32 v10, v10, v11
	s_nop 1
	v_mov_b32_dpp v11, v10 row_half_mirror row_mask:0xf bank_mask:0xf
	s_waitcnt lgkmcnt(3)
	v_add_f32_e32 v12, v12, v13
	s_nop 1
	v_mov_b32_dpp v13, v12 row_half_mirror row_mask:0xf bank_mask:0xf
	v_add_f32_e32 v2, v224, v2
	v_add_f32_e32 v3, v225, v3
	s_waitcnt lgkmcnt(1)
	v_add_f32_e32 v10, v10, v11
	s_nop 1
	v_mov_b32_dpp v11, v10 row_mirror row_mask:0xf bank_mask:0xf
	v_add_f32_e32 v6, v223, v6
	v_add_f32_e32 v8, v222, v8
	v_mov_b32_dpp v4, v2 quad_perm:[2,3,0,1] row_mask:0xf bank_mask:0xf
	v_mov_b32_dpp v5, v3 quad_perm:[2,3,0,1] row_mask:0xf bank_mask:0xf
	s_waitcnt lgkmcnt(2)
	v_add_f32_e32 v10, v10, v11
	v_mov_b32_e32 v11, v10
	s_nop 1
	v_permlane16_swap_b32_e32 v10, v11
	v_add_f32_e32 v19, v10, v11
	v_add_f32_e32 v10, v12, v13
	v_add_f32_e32 v12, v217, v14
	s_nop 1
	v_mov_b32_dpp v13, v12 quad_perm:[2,3,0,1] row_mask:0xf bank_mask:0xf
	v_mov_b32_dpp v11, v10 row_mirror row_mask:0xf bank_mask:0xf
	v_mov_b32_dpp v14, v215 quad_perm:[1,0,3,2] row_mask:0xf bank_mask:0xf
	v_mov_b32_dpp v7, v6 quad_perm:[2,3,0,1] row_mask:0xf bank_mask:0xf
	v_mov_b32_dpp v9, v8 quad_perm:[2,3,0,1] row_mask:0xf bank_mask:0xf
	s_waitcnt lgkmcnt(4)
	v_add_f32_e32 v12, v12, v13
	s_nop 1
	v_mov_b32_dpp v13, v12 row_half_mirror row_mask:0xf bank_mask:0xf
	s_waitcnt lgkmcnt(4)
	v_add_f32_e32 v10, v10, v11
	v_mov_b32_e32 v11, v10
	s_nop 1
	v_permlane16_swap_b32_e32 v10, v11
	v_add_f32_e32 v97, v10, v11
	s_waitcnt lgkmcnt(0)
	v_add_f32_e32 v10, v12, v13
	v_add_f32_e32 v12, v215, v14
	s_nop 1
	v_mov_b32_dpp v13, v12 quad_perm:[2,3,0,1] row_mask:0xf bank_mask:0xf
	v_mov_b32_dpp v11, v10 row_mirror row_mask:0xf bank_mask:0xf
	v_mov_b32_dpp v14, v220 quad_perm:[1,0,3,2] row_mask:0xf bank_mask:0xf
	v_add_f32_e32 v2, v2, v4
	v_add_f32_e32 v3, v3, v5
	s_waitcnt lgkmcnt(2)
	v_add_f32_e32 v12, v12, v13
	s_nop 1
	v_mov_b32_dpp v13, v12 row_half_mirror row_mask:0xf bank_mask:0xf
	s_waitcnt lgkmcnt(2)
	v_add_f32_e32 v10, v10, v11
	v_mov_b32_e32 v11, v10
	s_nop 1
	v_permlane16_swap_b32_e32 v10, v11
	v_add_f32_e32 v21, v10, v11
	s_waitcnt lgkmcnt(0)
	v_add_f32_e32 v10, v12, v13
	v_add_f32_e32 v12, v220, v14
	s_nop 1
	v_mov_b32_dpp v13, v12 quad_perm:[2,3,0,1] row_mask:0xf bank_mask:0xf
	v_mov_b32_dpp v11, v10 row_mirror row_mask:0xf bank_mask:0xf
	v_mov_b32_dpp v14, v218 quad_perm:[1,0,3,2] row_mask:0xf bank_mask:0xf
	v_add_f32_e32 v6, v6, v7
	v_add_f32_e32 v8, v8, v9
	s_waitcnt lgkmcnt(2)
	v_add_f32_e32 v12, v12, v13
	s_nop 1
	v_mov_b32_dpp v13, v12 row_half_mirror row_mask:0xf bank_mask:0xf
	s_waitcnt lgkmcnt(2)
	v_add_f32_e32 v10, v10, v11
	v_mov_b32_e32 v11, v10
	s_nop 1
	v_permlane16_swap_b32_e32 v10, v11
	v_add_f32_e32 v99, v10, v11
	s_waitcnt lgkmcnt(0)
	v_add_f32_e32 v10, v12, v13
	v_add_f32_e32 v12, v218, v14
	s_nop 1
	v_mov_b32_dpp v13, v12 quad_perm:[2,3,0,1] row_mask:0xf bank_mask:0xf
	v_mov_b32_dpp v11, v10 row_mirror row_mask:0xf bank_mask:0xf
	v_mov_b32_dpp v14, v216 quad_perm:[1,0,3,2] row_mask:0xf bank_mask:0xf
	v_mov_b32_dpp v4, v2 row_half_mirror row_mask:0xf bank_mask:0xf
	v_mov_b32_dpp v5, v3 row_half_mirror row_mask:0xf bank_mask:0xf
	s_waitcnt lgkmcnt(4)
	v_add_f32_e32 v12, v12, v13
	s_nop 1
	v_mov_b32_dpp v13, v12 row_half_mirror row_mask:0xf bank_mask:0xf
	s_waitcnt lgkmcnt(4)
	v_add_f32_e32 v10, v10, v11
	v_mov_b32_e32 v11, v10
	s_nop 1
	v_permlane16_swap_b32_e32 v10, v11
	v_add_f32_e32 v95, v10, v11
	s_waitcnt lgkmcnt(0)
	v_add_f32_e32 v10, v12, v13
	v_add_f32_e32 v12, v216, v14
	s_nop 1
	v_mov_b32_dpp v13, v12 quad_perm:[2,3,0,1] row_mask:0xf bank_mask:0xf
	v_mov_b32_dpp v11, v10 row_mirror row_mask:0xf bank_mask:0xf
	v_mov_b32_dpp v14, v214 quad_perm:[1,0,3,2] row_mask:0xf bank_mask:0xf
	v_mov_b32_dpp v7, v6 row_half_mirror row_mask:0xf bank_mask:0xf
	v_mov_b32_dpp v9, v8 row_half_mirror row_mask:0xf bank_mask:0xf
	s_waitcnt lgkmcnt(4)
	v_add_f32_e32 v12, v12, v13
	s_nop 1
	v_mov_b32_dpp v13, v12 row_half_mirror row_mask:0xf bank_mask:0xf
	s_waitcnt lgkmcnt(4)
	v_add_f32_e32 v10, v10, v11
	v_mov_b32_e32 v11, v10
	s_nop 1
	v_permlane16_swap_b32_e32 v10, v11
	v_add_f32_e32 v101, v10, v11
	s_waitcnt lgkmcnt(0)
	v_add_f32_e32 v10, v12, v13
	v_add_f32_e32 v12, v214, v14
	s_nop 1
	v_mov_b32_dpp v13, v12 quad_perm:[2,3,0,1] row_mask:0xf bank_mask:0xf
	v_mov_b32_dpp v11, v10 row_mirror row_mask:0xf bank_mask:0xf
	v_mov_b32_dpp v14, v213 quad_perm:[1,0,3,2] row_mask:0xf bank_mask:0xf
	v_add_f32_e32 v2, v2, v4
	v_add_f32_e32 v3, v3, v5
	s_waitcnt lgkmcnt(2)
	v_add_f32_e32 v12, v12, v13
	s_nop 1
	v_mov_b32_dpp v13, v12 row_half_mirror row_mask:0xf bank_mask:0xf
	s_waitcnt lgkmcnt(2)
	v_add_f32_e32 v10, v10, v11
	v_mov_b32_e32 v11, v10
	s_nop 1
	v_permlane16_swap_b32_e32 v10, v11
	v_add_f32_e32 v107, v10, v11
	s_waitcnt lgkmcnt(0)
	v_add_f32_e32 v10, v12, v13
	v_add_f32_e32 v12, v213, v14
	s_nop 1
	v_mov_b32_dpp v13, v12 quad_perm:[2,3,0,1] row_mask:0xf bank_mask:0xf
	v_mov_b32_dpp v11, v10 row_mirror row_mask:0xf bank_mask:0xf
	v_mov_b32_dpp v14, v212 quad_perm:[1,0,3,2] row_mask:0xf bank_mask:0xf
	v_add_f32_e32 v6, v6, v7
	v_add_f32_e32 v8, v8, v9
	s_waitcnt lgkmcnt(2)
	v_add_f32_e32 v12, v12, v13
	s_nop 1
	v_mov_b32_dpp v13, v12 row_half_mirror row_mask:0xf bank_mask:0xf
	s_waitcnt lgkmcnt(2)
	v_add_f32_e32 v10, v10, v11
	v_mov_b32_e32 v11, v10
	s_nop 1
	v_permlane16_swap_b32_e32 v10, v11
	v_add_f32_e32 v115, v10, v11
	s_waitcnt lgkmcnt(0)
	v_add_f32_e32 v10, v12, v13
	v_add_f32_e32 v12, v212, v14
	s_nop 1
	v_mov_b32_dpp v13, v12 quad_perm:[2,3,0,1] row_mask:0xf bank_mask:0xf
	v_mov_b32_dpp v11, v10 row_mirror row_mask:0xf bank_mask:0xf
	v_mov_b32_dpp v14, v211 quad_perm:[1,0,3,2] row_mask:0xf bank_mask:0xf
	v_mov_b32_dpp v4, v2 row_mirror row_mask:0xf bank_mask:0xf
	v_mov_b32_dpp v5, v3 row_mirror row_mask:0xf bank_mask:0xf
	s_waitcnt lgkmcnt(4)
	v_add_f32_e32 v12, v12, v13
	s_nop 1
	v_mov_b32_dpp v13, v12 row_half_mirror row_mask:0xf bank_mask:0xf
	s_waitcnt lgkmcnt(4)
	v_add_f32_e32 v10, v10, v11
	v_mov_b32_e32 v11, v10
	s_nop 1
	v_permlane16_swap_b32_e32 v10, v11
	v_add_f32_e32 v104, v10, v11
	s_waitcnt lgkmcnt(0)
	v_add_f32_e32 v10, v12, v13
	v_add_f32_e32 v12, v211, v14
	s_nop 1
	v_mov_b32_dpp v13, v12 quad_perm:[2,3,0,1] row_mask:0xf bank_mask:0xf
	v_mov_b32_dpp v11, v10 row_mirror row_mask:0xf bank_mask:0xf
	v_mov_b32_dpp v14, v210 quad_perm:[1,0,3,2] row_mask:0xf bank_mask:0xf
	v_mov_b32_dpp v7, v6 row_mirror row_mask:0xf bank_mask:0xf
	v_mov_b32_dpp v9, v8 row_mirror row_mask:0xf bank_mask:0xf
	s_waitcnt lgkmcnt(4)
	v_add_f32_e32 v12, v12, v13
	s_nop 1
	v_mov_b32_dpp v13, v12 row_half_mirror row_mask:0xf bank_mask:0xf
	s_waitcnt lgkmcnt(4)
	v_add_f32_e32 v10, v10, v11
	v_mov_b32_e32 v11, v10
	s_nop 1
	v_permlane16_swap_b32_e32 v10, v11
	v_add_f32_e32 v113, v10, v11
	s_waitcnt lgkmcnt(0)
	v_add_f32_e32 v10, v12, v13
	v_add_f32_e32 v12, v210, v14
	s_nop 1
	v_mov_b32_dpp v13, v12 quad_perm:[2,3,0,1] row_mask:0xf bank_mask:0xf
	v_mov_b32_dpp v11, v10 row_mirror row_mask:0xf bank_mask:0xf
	v_mov_b32_dpp v14, v209 quad_perm:[1,0,3,2] row_mask:0xf bank_mask:0xf
	v_add_f32_e32 v2, v2, v4
	v_add_f32_e32 v4, v3, v5
	s_waitcnt lgkmcnt(2)
	v_add_f32_e32 v12, v12, v13
	s_nop 1
	v_mov_b32_dpp v13, v12 row_half_mirror row_mask:0xf bank_mask:0xf
	s_waitcnt lgkmcnt(2)
	v_add_f32_e32 v10, v10, v11
	v_mov_b32_e32 v11, v10
	s_nop 1
	v_permlane16_swap_b32_e32 v10, v11
	v_add_f32_e32 v109, v10, v11
	s_waitcnt lgkmcnt(0)
	v_add_f32_e32 v10, v12, v13
	v_add_f32_e32 v12, v209, v14
	s_nop 1
	v_mov_b32_dpp v13, v12 quad_perm:[2,3,0,1] row_mask:0xf bank_mask:0xf
	v_mov_b32_dpp v11, v10 row_mirror row_mask:0xf bank_mask:0xf
	v_mov_b32_dpp v14, v208 quad_perm:[1,0,3,2] row_mask:0xf bank_mask:0xf
	v_add_f32_e32 v6, v6, v7
	v_add_f32_e32 v8, v8, v9
	s_waitcnt lgkmcnt(2)
	v_add_f32_e32 v12, v12, v13
	s_nop 1
	v_mov_b32_dpp v13, v12 row_half_mirror row_mask:0xf bank_mask:0xf
	s_waitcnt lgkmcnt(2)
	v_add_f32_e32 v10, v10, v11
	v_mov_b32_e32 v11, v10
	s_nop 1
	v_permlane16_swap_b32_e32 v10, v11
	v_add_f32_e32 v117, v10, v11
	s_waitcnt lgkmcnt(0)
	v_add_f32_e32 v10, v12, v13
	v_add_f32_e32 v12, v208, v14
	s_nop 1
	v_mov_b32_dpp v13, v12 quad_perm:[2,3,0,1] row_mask:0xf bank_mask:0xf
	v_mov_b32_dpp v11, v10 row_mirror row_mask:0xf bank_mask:0xf
	v_mov_b32_dpp v14, v207 quad_perm:[1,0,3,2] row_mask:0xf bank_mask:0xf
	v_mov_b32_e32 v3, v2
	v_mov_b32_e32 v5, v4
	s_waitcnt lgkmcnt(2)
	v_add_f32_e32 v12, v12, v13
	s_nop 1
	v_mov_b32_dpp v13, v12 row_half_mirror row_mask:0xf bank_mask:0xf
	s_waitcnt lgkmcnt(2)
	v_add_f32_e32 v10, v10, v11
	v_mov_b32_e32 v11, v10
	s_nop 1
	v_permlane16_swap_b32_e32 v10, v11
	v_add_f32_e32 v111, v10, v11
	s_waitcnt lgkmcnt(0)
	v_add_f32_e32 v10, v12, v13
	v_add_f32_e32 v12, v207, v14
	s_nop 1
	v_mov_b32_dpp v13, v12 quad_perm:[2,3,0,1] row_mask:0xf bank_mask:0xf
	v_mov_b32_dpp v11, v10 row_mirror row_mask:0xf bank_mask:0xf
	v_mov_b32_dpp v14, v206 quad_perm:[1,0,3,2] row_mask:0xf bank_mask:0xf
	v_mov_b32_e32 v7, v6
	v_mov_b32_e32 v9, v8
	s_waitcnt lgkmcnt(2)
	v_add_f32_e32 v12, v12, v13
	s_nop 1
	v_mov_b32_dpp v13, v12 row_half_mirror row_mask:0xf bank_mask:0xf
	s_waitcnt lgkmcnt(2)
	v_add_f32_e32 v10, v10, v11
	v_mov_b32_e32 v11, v10
	s_nop 1
	v_permlane16_swap_b32_e32 v10, v11
	v_add_f32_e32 v119, v10, v11
	s_waitcnt lgkmcnt(0)
	v_add_f32_e32 v10, v12, v13
	v_add_f32_e32 v12, v206, v14
	s_nop 1
	v_mov_b32_dpp v13, v12 quad_perm:[2,3,0,1] row_mask:0xf bank_mask:0xf
	v_mov_b32_dpp v11, v10 row_mirror row_mask:0xf bank_mask:0xf
	v_mov_b32_dpp v14, v205 quad_perm:[1,0,3,2] row_mask:0xf bank_mask:0xf
	v_permlane16_swap_b32_e32 v2, v3
	s_waitcnt lgkmcnt(2)
	v_add_f32_e32 v12, v12, v13
	s_nop 1
	v_mov_b32_dpp v13, v12 row_half_mirror row_mask:0xf bank_mask:0xf
	s_waitcnt lgkmcnt(2)
	v_add_f32_e32 v10, v10, v11
	v_mov_b32_e32 v11, v10
	s_nop 1
	v_permlane16_swap_b32_e32 v10, v11
	v_add_f32_e32 v123, v10, v11
	s_waitcnt lgkmcnt(0)
	v_add_f32_e32 v10, v12, v13
	v_add_f32_e32 v12, v205, v14
	s_nop 1
	v_mov_b32_dpp v13, v12 quad_perm:[2,3,0,1] row_mask:0xf bank_mask:0xf
	v_mov_b32_dpp v11, v10 row_mirror row_mask:0xf bank_mask:0xf
	v_mov_b32_dpp v14, v158 quad_perm:[1,0,3,2] row_mask:0xf bank_mask:0xf
	v_permlane16_swap_b32_e32 v4, v5
	s_waitcnt lgkmcnt(2)
	v_add_f32_e32 v12, v12, v13
	s_nop 1
	v_mov_b32_dpp v13, v12 row_half_mirror row_mask:0xf bank_mask:0xf
	s_waitcnt lgkmcnt(2)
	v_add_f32_e32 v10, v10, v11
	v_mov_b32_e32 v11, v10
	s_nop 1
	v_permlane16_swap_b32_e32 v10, v11
	v_add_f32_e32 v130, v10, v11
	s_waitcnt lgkmcnt(0)
	v_add_f32_e32 v10, v12, v13
	v_add_f32_e32 v12, v158, v14
	s_nop 1
	v_mov_b32_dpp v13, v12 quad_perm:[2,3,0,1] row_mask:0xf bank_mask:0xf
	v_mov_b32_dpp v11, v10 row_mirror row_mask:0xf bank_mask:0xf
	v_mov_b32_dpp v14, v153 quad_perm:[1,0,3,2] row_mask:0xf bank_mask:0xf
	v_permlane16_swap_b32_e32 v6, v7
	s_waitcnt lgkmcnt(2)
	v_add_f32_e32 v12, v12, v13
	s_nop 1
	v_mov_b32_dpp v13, v12 row_half_mirror row_mask:0xf bank_mask:0xf
	s_waitcnt lgkmcnt(2)
	v_add_f32_e32 v10, v10, v11
	v_mov_b32_e32 v11, v10
	s_nop 1
	v_permlane16_swap_b32_e32 v10, v11
	v_add_f32_e32 v121, v10, v11
	s_waitcnt lgkmcnt(0)
	v_add_f32_e32 v10, v12, v13
	v_add_f32_e32 v12, v153, v14
	s_nop 1
	v_mov_b32_dpp v13, v12 quad_perm:[2,3,0,1] row_mask:0xf bank_mask:0xf
	v_mov_b32_dpp v11, v10 row_mirror row_mask:0xf bank_mask:0xf
	v_mov_b32_dpp v14, v57 quad_perm:[1,0,3,2] row_mask:0xf bank_mask:0xf
	v_permlane16_swap_b32_e32 v8, v9
	s_waitcnt lgkmcnt(2)
	v_add_f32_e32 v12, v12, v13
	s_nop 1
	v_mov_b32_dpp v13, v12 row_half_mirror row_mask:0xf bank_mask:0xf
	s_waitcnt lgkmcnt(2)
	v_add_f32_e32 v10, v10, v11
	v_mov_b32_e32 v11, v10
	s_nop 1
	v_permlane16_swap_b32_e32 v10, v11
	v_add_f32_e32 v128, v10, v11
	s_waitcnt lgkmcnt(0)
	v_add_f32_e32 v10, v12, v13
	v_add_f32_e32 v12, v57, v14
	s_nop 1
	v_mov_b32_dpp v13, v12 quad_perm:[2,3,0,1] row_mask:0xf bank_mask:0xf
	v_mov_b32_dpp v11, v10 row_mirror row_mask:0xf bank_mask:0xf
	v_mov_b32_dpp v14, v159 quad_perm:[1,0,3,2] row_mask:0xf bank_mask:0xf
	v_add_f32_e32 v2, v2, v3
	v_add_f32_e32 v4, v4, v5
	s_waitcnt lgkmcnt(2)
	v_add_f32_e32 v12, v12, v13
	s_nop 1
	v_mov_b32_dpp v13, v12 row_half_mirror row_mask:0xf bank_mask:0xf
	s_waitcnt lgkmcnt(2)
	v_add_f32_e32 v10, v10, v11
	v_mov_b32_e32 v11, v10
	s_nop 1
	v_permlane16_swap_b32_e32 v10, v11
	v_add_f32_e32 v57, v10, v11
	s_waitcnt lgkmcnt(0)
	v_add_f32_e32 v10, v12, v13
	v_add_f32_e32 v12, v159, v14
	s_nop 1
	v_mov_b32_dpp v13, v12 quad_perm:[2,3,0,1] row_mask:0xf bank_mask:0xf
	v_mov_b32_dpp v11, v10 row_mirror row_mask:0xf bank_mask:0xf
	v_mov_b32_dpp v14, v156 quad_perm:[1,0,3,2] row_mask:0xf bank_mask:0xf
	v_add_f32_e32 v6, v6, v7
	v_add_f32_e32 v8, v8, v9
	s_waitcnt lgkmcnt(2)
	v_add_f32_e32 v12, v12, v13
	s_nop 1
	v_mov_b32_dpp v13, v12 row_half_mirror row_mask:0xf bank_mask:0xf
	s_waitcnt lgkmcnt(2)
	v_add_f32_e32 v10, v10, v11
	v_mov_b32_e32 v11, v10
	s_nop 1
	v_permlane16_swap_b32_e32 v10, v11
	v_add_f32_e32 v132, v10, v11
	s_waitcnt lgkmcnt(0)
	v_add_f32_e32 v10, v12, v13
	v_add_f32_e32 v12, v156, v14
	s_nop 1
	v_mov_b32_dpp v13, v12 quad_perm:[2,3,0,1] row_mask:0xf bank_mask:0xf
	v_mov_b32_dpp v11, v10 row_mirror row_mask:0xf bank_mask:0xf
	v_mov_b32_dpp v14, v152 quad_perm:[1,0,3,2] row_mask:0xf bank_mask:0xf
	v_mov_b32_e32 v3, v2
	v_mov_b32_e32 v5, v4
	s_waitcnt lgkmcnt(2)
	v_add_f32_e32 v12, v12, v13
	s_nop 1
	v_mov_b32_dpp v13, v12 row_half_mirror row_mask:0xf bank_mask:0xf
	s_waitcnt lgkmcnt(2)
	v_add_f32_e32 v10, v10, v11
	v_mov_b32_e32 v11, v10
	s_nop 1
	v_permlane16_swap_b32_e32 v10, v11
	v_add_f32_e32 v126, v10, v11
	s_waitcnt lgkmcnt(0)
	v_add_f32_e32 v10, v12, v13
	v_add_f32_e32 v12, v152, v14
	s_nop 1
	v_mov_b32_dpp v13, v12 quad_perm:[2,3,0,1] row_mask:0xf bank_mask:0xf
	v_mov_b32_dpp v11, v10 row_mirror row_mask:0xf bank_mask:0xf
	v_mov_b32_dpp v14, v55 quad_perm:[1,0,3,2] row_mask:0xf bank_mask:0xf
	v_mov_b32_e32 v7, v6
	v_mov_b32_e32 v9, v8
	s_waitcnt lgkmcnt(2)
	v_add_f32_e32 v12, v12, v13
	s_nop 1
	v_mov_b32_dpp v13, v12 row_half_mirror row_mask:0xf bank_mask:0xf
	s_waitcnt lgkmcnt(2)
	v_add_f32_e32 v10, v10, v11
	v_mov_b32_e32 v11, v10
	s_nop 1
	v_permlane16_swap_b32_e32 v10, v11
	v_add_f32_e32 v134, v10, v11
	s_waitcnt lgkmcnt(0)
	v_add_f32_e32 v10, v12, v13
	v_add_f32_e32 v12, v55, v14
	s_nop 1
	v_mov_b32_dpp v13, v12 quad_perm:[2,3,0,1] row_mask:0xf bank_mask:0xf
	v_mov_b32_dpp v11, v10 row_mirror row_mask:0xf bank_mask:0xf
	v_mov_b32_dpp v14, v53 quad_perm:[1,0,3,2] row_mask:0xf bank_mask:0xf
	v_mov_b32_e32 v20, v19
	v_mov_b32_e32 v98, v97
	s_waitcnt lgkmcnt(2)
	v_add_f32_e32 v12, v12, v13
	s_nop 1
	v_mov_b32_dpp v13, v12 row_half_mirror row_mask:0xf bank_mask:0xf
	s_waitcnt lgkmcnt(2)
	v_add_f32_e32 v10, v10, v11
	v_mov_b32_e32 v11, v10
	s_nop 1
	v_permlane16_swap_b32_e32 v10, v11
	v_add_f32_e32 v55, v10, v11
	s_waitcnt lgkmcnt(0)
	v_add_f32_e32 v10, v12, v13
	v_add_f32_e32 v12, v53, v14
	s_nop 1
	v_mov_b32_dpp v13, v12 quad_perm:[2,3,0,1] row_mask:0xf bank_mask:0xf
	v_mov_b32_dpp v11, v10 row_mirror row_mask:0xf bank_mask:0xf
	v_mov_b32_dpp v14, v51 quad_perm:[1,0,3,2] row_mask:0xf bank_mask:0xf
	v_mov_b32_e32 v94, v21
	v_mov_b32_e32 v100, v99
	s_waitcnt lgkmcnt(2)
	v_add_f32_e32 v12, v12, v13
	s_nop 1
	v_mov_b32_dpp v13, v12 row_half_mirror row_mask:0xf bank_mask:0xf
	s_waitcnt lgkmcnt(2)
	v_add_f32_e32 v10, v10, v11
	v_mov_b32_e32 v11, v10
	s_nop 1
	v_permlane16_swap_b32_e32 v10, v11
	v_add_f32_e32 v143, v10, v11
	s_waitcnt lgkmcnt(0)
	v_add_f32_e32 v10, v12, v13
	v_add_f32_e32 v12, v51, v14
	s_nop 0
	v_mov_b32_dpp v11, v10 row_mirror row_mask:0xf bank_mask:0xf
	s_nop 0
	v_mov_b32_dpp v13, v12 quad_perm:[2,3,0,1] row_mask:0xf bank_mask:0xf
	v_mov_b32_dpp v14, v47 quad_perm:[1,0,3,2] row_mask:0xf bank_mask:0xf
	v_mov_b32_e32 v96, v95
	v_mov_b32_e32 v102, v101
	s_waitcnt lgkmcnt(2)
	v_add_f32_e32 v10, v10, v11
	s_waitcnt lgkmcnt(1)
	v_add_f32_e32 v11, v12, v13
	s_nop 1
	v_mov_b32_dpp v12, v11 row_half_mirror row_mask:0xf bank_mask:0xf
	v_mov_b32_e32 v13, v10
	s_nop 1
	v_permlane16_swap_b32_e32 v10, v13
	v_add_f32_e32 v51, v10, v13
	s_waitcnt lgkmcnt(0)
	v_add_f32_e32 v10, v11, v12
	s_nop 1
	v_mov_b32_dpp v11, v10 row_mirror row_mask:0xf bank_mask:0xf
	v_mov_b32_dpp v12, v49 quad_perm:[1,0,3,2] row_mask:0xf bank_mask:0xf
	v_mov_b32_e32 v108, v107
	v_mov_b32_e32 v116, v115
	v_mov_b32_e32 v106, v104
	s_waitcnt lgkmcnt(1)
	v_add_f32_e32 v10, v10, v11
	s_waitcnt lgkmcnt(0)
	v_add_f32_e32 v11, v49, v12
	v_mov_b32_e32 v13, v10
	s_nop 0
	v_mov_b32_dpp v12, v11 quad_perm:[2,3,0,1] row_mask:0xf bank_mask:0xf
	s_nop 0
	v_permlane16_swap_b32_e32 v10, v13
	v_add_f32_e32 v141, v10, v13
	v_add_f32_e32 v10, v47, v14
	s_nop 1
	v_mov_b32_dpp v13, v10 quad_perm:[2,3,0,1] row_mask:0xf bank_mask:0xf
	s_waitcnt lgkmcnt(1)
	v_add_f32_e32 v11, v11, v12
	s_nop 1
	v_mov_b32_dpp v12, v11 row_half_mirror row_mask:0xf bank_mask:0xf
	v_mov_b32_e32 v114, v113
	v_mov_b32_e32 v110, v109
	s_waitcnt lgkmcnt(1)
	v_add_f32_e32 v10, v10, v13
	s_nop 1
	v_mov_b32_dpp v13, v10 row_half_mirror row_mask:0xf bank_mask:0xf
	s_waitcnt lgkmcnt(1)
	v_add_f32_e32 v11, v11, v12
	s_nop 1
	v_mov_b32_dpp v12, v11 row_mirror row_mask:0xf bank_mask:0xf
	v_mov_b32_e32 v118, v117
	v_mov_b32_e32 v112, v111
	s_waitcnt lgkmcnt(1)
	v_add_f32_e32 v10, v10, v13
	s_nop 1
	v_mov_b32_dpp v13, v10 row_mirror row_mask:0xf bank_mask:0xf
	s_waitcnt lgkmcnt(1)
	v_add_f32_e32 v11, v11, v12
	v_mov_b32_e32 v12, v11
	s_nop 1
	v_permlane16_swap_b32_e32 v11, v12
	s_waitcnt lgkmcnt(0)
	v_add_f32_e32 v10, v10, v13
	v_add_f32_e32 v136, v11, v12
	v_mov_b32_e32 v11, v10
	s_nop 1
	v_permlane16_swap_b32_e32 v10, v11
	v_add_f32_e32 v139, v10, v11
	v_mov_b32_e32 v120, v119
	v_mov_b32_e32 v124, v123
	v_mov_b32_e32 v131, v130
	v_mov_b32_e32 v122, v121
	v_mov_b32_e32 v129, v128
	v_mov_b32_e32 v125, v57
	v_mov_b32_e32 v133, v132
	v_mov_b32_e32 v127, v126
	v_mov_b32_e32 v135, v134
	v_mov_b32_e32 v137, v55
	v_mov_b32_e32 v144, v143
	v_mov_b32_e32 v53, v51
	v_mov_b32_e32 v142, v141
	v_mov_b32_e32 v138, v136
	v_mov_b32_e32 v140, v139
	v_permlane32_swap_b32_e32 v2, v3
	v_permlane32_swap_b32_e32 v4, v5
	v_permlane32_swap_b32_e32 v6, v7
	v_permlane32_swap_b32_e32 v8, v9
	v_permlane32_swap_b32_e32 v19, v20
	v_permlane32_swap_b32_e32 v97, v98
	v_permlane32_swap_b32_e32 v21, v94
	v_permlane32_swap_b32_e32 v99, v100
	v_permlane32_swap_b32_e32 v95, v96
	v_permlane32_swap_b32_e32 v101, v102
	v_permlane32_swap_b32_e32 v107, v108
	v_permlane32_swap_b32_e32 v115, v116
	v_permlane32_swap_b32_e32 v104, v106
	v_permlane32_swap_b32_e32 v113, v114
	v_permlane32_swap_b32_e32 v109, v110
	v_permlane32_swap_b32_e32 v117, v118
	v_permlane32_swap_b32_e32 v111, v112
	v_permlane32_swap_b32_e32 v119, v120
	v_permlane32_swap_b32_e32 v123, v124
	v_permlane32_swap_b32_e32 v130, v131
	v_permlane32_swap_b32_e32 v121, v122
	v_permlane32_swap_b32_e32 v128, v129
	v_permlane32_swap_b32_e32 v57, v125
	v_permlane32_swap_b32_e32 v132, v133
	v_permlane32_swap_b32_e32 v126, v127
	v_permlane32_swap_b32_e32 v134, v135
	v_permlane32_swap_b32_e32 v55, v137
	v_permlane32_swap_b32_e32 v143, v144
	v_permlane32_swap_b32_e32 v51, v53
	v_permlane32_swap_b32_e32 v141, v142
	v_permlane32_swap_b32_e32 v136, v138
	v_permlane32_swap_b32_e32 v139, v140
	s_and_saveexec_b64 s[4:5], s[42:43]
	s_cbranch_execz .LBB0_1299
	v_add_f32_e32 v4, v4, v5
	v_add_f32_e32 v2, v2, v3
	v_cndmask_b32_e64 v2, v2, v4, s[40:41]
	v_mul_f32_e32 v2, 0xbfb8aa3b, v2
	s_load_dwordx2 s[6:7], s[56:57], 0xd0
	v_exp_f32_e32 v2, v2
	v_add_f32_e32 v8, v8, v9
	v_add_f32_e32 v6, v6, v7
	v_cndmask_b32_e64 v49, v6, v8, s[40:41]
	v_add_f32_e32 v2, 1.0, v2
	v_rcp_f32_e32 v18, v2
	s_waitcnt lgkmcnt(0)
	global_load_dwordx4 v[2:5], v1, s[6:7] offset:48
	global_load_dwordx4 v[6:9], v1, s[6:7] offset:32
	global_load_dwordx4 v[10:13], v1, s[6:7] offset:16
	global_load_dwordx4 v[14:17], v1, s[6:7]
	s_mov_b32 s6, 0xf149f2ca
	s_waitcnt vmcnt(0)
	v_add_f32_e32 v47, v18, v14
	v_mul_f32_e32 v14, 0xbfb8aa3b, v49
	v_exp_f32_e32 v14, v14
	v_cmp_nlt_f32_e32 vcc, s6, v47
	v_add_f32_e32 v14, 1.0, v14
	v_rcp_f32_e32 v14, v14
	s_nop 0
	v_add_f32_e32 v49, v14, v15
	v_mov_b32_e32 v15, 0xf149f2ca
	v_cndmask_b32_e32 v145, v47, v15, vcc
	v_cmp_gt_f32_e64 s[44:45], v49, v145
	v_cmp_ngt_f32_e64 s[46:47], v49, v145
	v_mov_b32_e32 v148, v49
	v_mov_b32_e32 v147, v145
	s_and_saveexec_b64 s[6:7], s[46:47]
	s_cbranch_execz .LBB0_1305
	v_mov_b32_e32 v147, 0xf149f2ca
	v_cmp_gt_f32_e64 s[46:47], v49, v147
	s_and_saveexec_b64 s[8:9], s[46:47]
	v_mov_b32_e32 v147, v49
	s_or_b64 exec, exec, s[8:9]
	v_mov_b32_e32 v148, v145
